# gemm8: main loop split into two copies by wave half; waves 4-7 run every s_setprio one level higher (static priority raise for the younger half)
# baseline (speedup 1.0000x reference)
_Z5gemm8ILi0EEvPKtS1_ii7EpiArgs:
	s_load_dwordx4 s[8:11], s[0:1], 0x0
	s_waitcnt lgkmcnt(0)
	s_and_b32 s3, s2, 7
	s_lshr_b32 s6, s2, 3
	s_lshr_b32 s7, s3, 1
	s_lshl_b32 s7, s7, 2
	s_lshr_b32 s12, s6, 3
	s_add_i32 s7, s7, s12
	s_and_b32 s3, s3, 1
	s_lshl_b32 s3, s3, 2
	s_and_b32 s12, s6, 3
	s_add_i32 s3, s3, s12
	s_bfe_u32 s12, s6, 0x10002
	s_lshl_b32 s12, s12, 3
	s_add_i32 s24, s3, s12
	v_and_b32_e32 v2, 32, v0
	v_bfe_u32 v14, v0, 2, 4
	v_and_b32_e32 v16, 64, v0
	v_mov_b32_e32 v131, 0
	v_mov_b32_e32 v19, v131
	v_mov_b32_e32 v21, v131
	v_lshrrev_b32_e32 v145, 8, v0
	s_ashr_i32 s25, s24, 2
	s_cmp_eq_u32 s25, 2
	s_cselect_b64 s[4:5], -1, 0
	s_and_b64 s[2:3], s[4:5], exec
	s_cselect_b32 s2, s24, s7
	s_cselect_b32 s20, s9, s11
	s_cselect_b32 s21, s8, s10
	s_cselect_b32 s14, s7, s24
	s_lshl_b32 s6, s2, 8
	s_ashr_i32 s7, s6, 31
	s_lshl_b64 s[2:3], s[6:7], 11
	s_add_u32 s12, s21, s2
	v_lshlrev_b32_e32 v1, 4, v0
	s_addc_u32 s13, s20, s3
	s_add_i32 s22, 0, 0x10000
	v_add_u32_e32 v152, s22, v1
	v_or_b32_e32 v17, 0x2000, v1
	v_readfirstlane_b32 s7, v152
	v_bitop3_b32 v15, v1, v2, 48 bitop3:0x6c
	v_lshrrev_b32_e32 v2, 3, v0
	s_mov_b32 m0, s7
	v_lshrrev_b32_e32 v6, 7, v17
	s_movk_i32 s7, 0x70
	v_or_b32_e32 v130, v15, v16
	v_and_or_b32 v2, v2, 48, v14
	v_and_or_b32 v6, v6, s7, v14
	v_lshl_add_u64 v[4:5], s[12:13], 0, v[130:131]
	v_lshlrev_b32_e32 v18, 11, v2
	v_lshlrev_b32_e32 v20, 11, v6
	v_add_u32_e32 v6, s22, v17
	v_lshl_add_u64 v[2:3], v[4:5], 0, v[18:19]
	v_readfirstlane_b32 s7, v6
	v_lshrrev_b32_e32 v246, 6, v0
	s_mov_b64 s[34:35], 0x10000
	s_nop 0
	v_readfirstlane_b32 s40, v246
	s_cmp_ge_u32 s40, 4
	s_cbranch_scc1 .Lg8b_entry
	s_and_b64 s[12:13], s[4:5], exec
	global_load_lds_dwordx4 v[2:3], off
	s_mov_b32 m0, s7
	s_cselect_b32 s7, s11, s9
	s_cselect_b32 s23, s10, s8
	s_lshl_b32 s12, s14, 8
	s_ashr_i32 s13, s12, 31
	s_lshl_b64 s[18:19], s[12:13], 11
	s_add_u32 s8, s23, s18
	s_addc_u32 s9, s7, s19
	v_add_u32_e32 v153, 0, v1
	v_lshl_add_u64 v[4:5], v[4:5], 0, v[20:21]
	v_lshl_add_u64 v[8:9], s[8:9], 0, v[130:131]
	v_readfirstlane_b32 s8, v153
	v_add_u32_e32 v155, 0x2000, v153
	global_load_lds_dwordx4 v[4:5], off
	v_lshl_add_u64 v[6:7], v[8:9], 0, v[18:19]
	s_mov_b32 m0, s8
	v_readfirstlane_b32 s8, v155
	global_load_lds_dwordx4 v[6:7], off
	s_mov_b32 m0, s8
	s_or_b32 s8, s6, 0x80
	s_ashr_i32 s9, s8, 31
	s_lshl_b64 s[8:9], s[8:9], 11
	s_add_u32 s8, s21, s8
	s_addc_u32 s9, s20, s9
	s_add_i32 s13, 0, 0x14000
	v_add_u32_e32 v156, s13, v1
	v_lshl_add_u64 v[8:9], v[8:9], 0, v[20:21]
	v_lshl_add_u64 v[12:13], s[8:9], 0, v[130:131]
	v_readfirstlane_b32 s8, v156
	v_add_u32_e32 v22, s13, v17
	global_load_lds_dwordx4 v[8:9], off
	v_lshl_add_u64 v[10:11], v[12:13], 0, v[18:19]
	s_mov_b32 m0, s8
	v_readfirstlane_b32 s8, v22
	global_load_lds_dwordx4 v[10:11], off
	s_mov_b32 m0, s8
	s_or_b32 s8, s12, 0x80
	s_ashr_i32 s9, s8, 31
	s_lshl_b64 s[8:9], s[8:9], 11
	s_add_u32 s8, s23, s8
	s_addc_u32 s9, s7, s9
	v_add_u32_e32 v158, 0x4000, v153
	v_lshl_add_u64 v[12:13], v[12:13], 0, v[20:21]
	v_lshl_add_u64 v[22:23], s[8:9], 0, v[130:131]
	v_readfirstlane_b32 s8, v158
	v_add_u32_e32 v159, 0x6000, v153
	global_load_lds_dwordx4 v[12:13], off
	v_lshl_add_u64 v[132:133], v[22:23], 0, v[18:19]
	s_mov_b32 m0, s8
	v_readfirstlane_b32 s8, v159
	global_load_lds_dwordx4 v[132:133], off
	v_lshl_add_u64 v[134:135], v[22:23], 0, v[20:21]
	s_mov_b32 m0, s8
	v_cmp_eq_u32_e32 vcc, 1, v145
	global_load_lds_dwordx4 v[134:135], off
	s_load_dwordx2 s[16:17], s[0:1], 0x30
	s_load_dwordx2 s[14:15], s[0:1], 0x40
	s_and_saveexec_b64 s[8:9], vcc
	s_cbranch_execz .LBB15_6
	s_barrier

.LBB15_7:
	ds_read_b128 v[172:175], v167
	ds_read_b128 v[176:179], v167 offset:1024
	ds_read_b128 v[180:183], v167 offset:2048
	ds_read_b128 v[184:187], v167 offset:3072
	v_lshl_add_u64 v[236:237], v[138:139], 0, v[130:131]
	v_readfirstlane_b32 s13, v168
	v_lshl_add_u64 v[188:189], v[236:237], 0, s[0:1]
	s_mov_b32 m0, s13
	v_lshl_add_u64 v[238:239], v[136:137], 0, v[130:131]
	v_readfirstlane_b32 s13, v169
	global_load_lds_dwordx4 v[188:189], off
	v_lshl_add_u64 v[188:189], v[238:239], 0, s[0:1]
	s_mov_b32 m0, s13
	s_nop 0
	global_load_lds_dwordx4 v[188:189], off
	ds_read_b128 v[188:191], v151
	ds_read_b128 v[192:195], v151 offset:1024
	ds_read_b128 v[196:199], v150
	ds_read_b128 v[200:203], v150 offset:1024
	ds_read_b128 v[204:207], v149
	ds_read_b128 v[208:211], v149 offset:1024
	ds_read_b128 v[212:215], v148
	ds_read_b128 v[216:219], v148 offset:1024
	s_waitcnt lgkmcnt(8)
	s_barrier
	s_waitcnt lgkmcnt(0)
	s_setprio 1
	s_waitcnt lgkmcnt(0)
	v_mfma_f32_16x16x32_f16 v[126:129], v[188:191], v[172:175], v[126:129]
	v_mfma_f32_16x16x32_f16 v[122:125], v[188:191], v[180:183], v[122:125]
	v_mfma_f32_16x16x32_f16 v[118:121], v[196:199], v[172:175], v[118:121]
	v_mfma_f32_16x16x32_f16 v[114:117], v[196:199], v[180:183], v[114:117]
	v_mfma_f32_16x16x32_f16 v[110:113], v[204:207], v[172:175], v[110:113]
	v_mfma_f32_16x16x32_f16 v[106:109], v[204:207], v[180:183], v[106:109]
	v_mfma_f32_16x16x32_f16 v[102:105], v[212:215], v[172:175], v[102:105]
	v_mfma_f32_16x16x32_f16 v[98:101], v[212:215], v[180:183], v[98:101]
	v_mfma_f32_16x16x32_f16 v[126:129], v[192:195], v[176:179], v[126:129]
	v_mfma_f32_16x16x32_f16 v[122:125], v[192:195], v[184:187], v[122:125]
	v_mfma_f32_16x16x32_f16 v[118:121], v[200:203], v[176:179], v[118:121]
	v_mfma_f32_16x16x32_f16 v[114:117], v[200:203], v[184:187], v[114:117]
	v_mfma_f32_16x16x32_f16 v[110:113], v[208:211], v[176:179], v[110:113]
	v_mfma_f32_16x16x32_f16 v[106:109], v[208:211], v[184:187], v[106:109]
	v_mfma_f32_16x16x32_f16 v[102:105], v[216:219], v[176:179], v[102:105]
	v_mfma_f32_16x16x32_f16 v[98:101], v[216:219], v[184:187], v[98:101]
	s_setprio 0
	s_barrier
	v_lshl_add_u64 v[240:241], v[142:143], 0, v[130:131]
	v_readfirstlane_b32 s13, v152
	v_lshl_add_u64 v[242:243], v[240:241], 0, s[2:3]
	s_mov_b32 m0, s13
	ds_read_b128 v[220:223], v166
	ds_read_b128 v[224:227], v166 offset:1024
	ds_read_b128 v[228:231], v166 offset:2048
	ds_read_b128 v[232:235], v166 offset:3072
	global_load_lds_dwordx4 v[242:243], off
	v_lshl_add_u64 v[242:243], v[140:141], 0, v[130:131]
	v_readfirstlane_b32 s13, v170
	v_lshl_add_u64 v[244:245], v[242:243], 0, s[2:3]
	s_mov_b32 m0, s13
	s_nop 0
	global_load_lds_dwordx4 v[244:245], off
	s_barrier
	s_waitcnt lgkmcnt(0)
	s_setprio 1
	s_waitcnt lgkmcnt(0)
	v_mfma_f32_16x16x32_f16 v[94:97], v[188:191], v[220:223], v[94:97]
	v_mfma_f32_16x16x32_f16 v[90:93], v[188:191], v[228:231], v[90:93]
	v_mfma_f32_16x16x32_f16 v[86:89], v[196:199], v[220:223], v[86:89]
	v_mfma_f32_16x16x32_f16 v[82:85], v[196:199], v[228:231], v[82:85]
	v_mfma_f32_16x16x32_f16 v[78:81], v[204:207], v[220:223], v[78:81]
	v_mfma_f32_16x16x32_f16 v[74:77], v[204:207], v[228:231], v[74:77]
	v_mfma_f32_16x16x32_f16 v[70:73], v[212:215], v[220:223], v[70:73]
	v_mfma_f32_16x16x32_f16 v[66:69], v[212:215], v[228:231], v[66:69]
	v_mfma_f32_16x16x32_f16 v[94:97], v[192:195], v[224:227], v[94:97]
	v_mfma_f32_16x16x32_f16 v[90:93], v[192:195], v[232:235], v[90:93]
	v_mfma_f32_16x16x32_f16 v[86:89], v[200:203], v[224:227], v[86:89]
	v_mfma_f32_16x16x32_f16 v[82:85], v[200:203], v[232:235], v[82:85]
	v_mfma_f32_16x16x32_f16 v[78:81], v[208:211], v[224:227], v[78:81]
	v_mfma_f32_16x16x32_f16 v[74:77], v[208:211], v[232:235], v[74:77]
	v_mfma_f32_16x16x32_f16 v[70:73], v[216:219], v[224:227], v[70:73]
	v_mfma_f32_16x16x32_f16 v[66:69], v[216:219], v[232:235], v[66:69]
	s_setprio 0
	v_readfirstlane_b32 s13, v153
	v_lshl_add_u64 v[244:245], v[236:237], 0, s[2:3]
	s_mov_b32 m0, s13
	v_readfirstlane_b32 s13, v155
	s_barrier
	ds_read_b128 v[188:191], v151 offset:16384
	ds_read_b128 v[192:195], v151 offset:17408
	ds_read_b128 v[196:199], v150 offset:16384
	ds_read_b128 v[200:203], v150 offset:17408
	ds_read_b128 v[204:207], v149 offset:16384
	ds_read_b128 v[208:211], v149 offset:17408
	ds_read_b128 v[212:215], v148 offset:16384
	ds_read_b128 v[216:219], v148 offset:17408
	global_load_lds_dwordx4 v[244:245], off
	v_lshl_add_u64 v[244:245], v[238:239], 0, s[2:3]
	s_mov_b32 m0, s13
	s_nop 0
	global_load_lds_dwordx4 v[244:245], off
	s_barrier
	s_waitcnt lgkmcnt(0)
	s_setprio 1
	s_waitcnt lgkmcnt(0)
	v_mfma_f32_16x16x32_f16 v[62:65], v[188:191], v[172:175], v[62:65]
	v_mfma_f32_16x16x32_f16 v[58:61], v[188:191], v[180:183], v[58:61]
	v_mfma_f32_16x16x32_f16 v[54:57], v[196:199], v[172:175], v[54:57]
	v_mfma_f32_16x16x32_f16 v[50:53], v[196:199], v[180:183], v[50:53]
	v_mfma_f32_16x16x32_f16 v[46:49], v[204:207], v[172:175], v[46:49]
	v_mfma_f32_16x16x32_f16 v[42:45], v[204:207], v[180:183], v[42:45]
	v_mfma_f32_16x16x32_f16 v[38:41], v[212:215], v[172:175], v[38:41]
	v_mfma_f32_16x16x32_f16 v[34:37], v[212:215], v[180:183], v[34:37]
	v_mfma_f32_16x16x32_f16 v[62:65], v[192:195], v[176:179], v[62:65]
	v_mfma_f32_16x16x32_f16 v[58:61], v[192:195], v[184:187], v[58:61]
	v_mfma_f32_16x16x32_f16 v[54:57], v[200:203], v[176:179], v[54:57]
	v_mfma_f32_16x16x32_f16 v[50:53], v[200:203], v[184:187], v[50:53]
	v_mfma_f32_16x16x32_f16 v[46:49], v[208:211], v[176:179], v[46:49]
	v_mfma_f32_16x16x32_f16 v[42:45], v[208:211], v[184:187], v[42:45]
	v_mfma_f32_16x16x32_f16 v[38:41], v[216:219], v[176:179], v[38:41]
	v_mfma_f32_16x16x32_f16 v[34:37], v[216:219], v[184:187], v[34:37]
	s_setprio 0
	s_barrier
	v_readfirstlane_b32 s13, v156
	v_lshl_add_u64 v[172:173], v[240:241], 0, s[18:19]
	s_mov_b32 m0, s13
	v_readfirstlane_b32 s13, v171
	global_load_lds_dwordx4 v[172:173], off
	v_lshl_add_u64 v[172:173], v[242:243], 0, s[18:19]
	s_mov_b32 m0, s13
	s_nop 0
	global_load_lds_dwordx4 v[172:173], off
	s_waitcnt vmcnt(6)
	s_barrier
	s_setprio 1
	v_mfma_f32_16x16x32_f16 v[30:33], v[188:191], v[220:223], v[30:33]
	v_mfma_f32_16x16x32_f16 v[26:29], v[188:191], v[228:231], v[26:29]
	v_mfma_f32_16x16x32_f16 v[22:25], v[196:199], v[220:223], v[22:25]
	v_mfma_f32_16x16x32_f16 v[18:21], v[196:199], v[228:231], v[18:21]
	v_mfma_f32_16x16x32_f16 v[14:17], v[204:207], v[220:223], v[14:17]
	v_mfma_f32_16x16x32_f16 v[10:13], v[204:207], v[228:231], v[10:13]
	v_mfma_f32_16x16x32_f16 v[6:9], v[212:215], v[220:223], v[6:9]
	v_mfma_f32_16x16x32_f16 v[2:5], v[212:215], v[228:231], v[2:5]
	v_mfma_f32_16x16x32_f16 v[30:33], v[192:195], v[224:227], v[30:33]
	v_mfma_f32_16x16x32_f16 v[26:29], v[192:195], v[232:235], v[26:29]
	v_mfma_f32_16x16x32_f16 v[22:25], v[200:203], v[224:227], v[22:25]
	v_mfma_f32_16x16x32_f16 v[18:21], v[200:203], v[232:235], v[18:21]
	v_mfma_f32_16x16x32_f16 v[14:17], v[208:211], v[224:227], v[14:17]
	v_mfma_f32_16x16x32_f16 v[10:13], v[208:211], v[232:235], v[10:13]
	v_mfma_f32_16x16x32_f16 v[6:9], v[216:219], v[224:227], v[6:9]
	v_mfma_f32_16x16x32_f16 v[2:5], v[216:219], v[232:235], v[2:5]
	s_setprio 0
	s_barrier
	ds_read_b128 v[172:175], v157
	ds_read_b128 v[176:179], v157 offset:1024
	ds_read_b128 v[180:183], v157 offset:2048
	ds_read_b128 v[184:187], v157 offset:3072
	v_readfirstlane_b32 s13, v158
	v_lshl_add_u64 v[220:221], v[236:237], 0, s[18:19]
	s_mov_b32 m0, s13
	v_readfirstlane_b32 s13, v159
	ds_read_b128 v[188:191], v151 offset:32768
	ds_read_b128 v[192:195], v151 offset:33792
	ds_read_b128 v[196:199], v150 offset:32768
	ds_read_b128 v[200:203], v150 offset:33792
	ds_read_b128 v[204:207], v149 offset:32768
	ds_read_b128 v[208:211], v149 offset:33792
	ds_read_b128 v[212:215], v148 offset:32768
	ds_read_b128 v[216:219], v148 offset:33792
	global_load_lds_dwordx4 v[220:221], off
	v_lshl_add_u64 v[220:221], v[238:239], 0, s[18:19]
	s_mov_b32 m0, s13
	s_nop 0
	global_load_lds_dwordx4 v[220:221], off
	s_waitcnt lgkmcnt(8)
	s_barrier
	s_waitcnt lgkmcnt(0)
	s_setprio 1
	s_waitcnt lgkmcnt(0)
	v_mfma_f32_16x16x32_f16 v[126:129], v[188:191], v[172:175], v[126:129]
	v_mfma_f32_16x16x32_f16 v[122:125], v[188:191], v[180:183], v[122:125]
	v_mfma_f32_16x16x32_f16 v[118:121], v[196:199], v[172:175], v[118:121]
	v_mfma_f32_16x16x32_f16 v[114:117], v[196:199], v[180:183], v[114:117]
	v_mfma_f32_16x16x32_f16 v[110:113], v[204:207], v[172:175], v[110:113]
	v_mfma_f32_16x16x32_f16 v[106:109], v[204:207], v[180:183], v[106:109]
	v_mfma_f32_16x16x32_f16 v[102:105], v[212:215], v[172:175], v[102:105]
	v_mfma_f32_16x16x32_f16 v[98:101], v[212:215], v[180:183], v[98:101]
	v_mfma_f32_16x16x32_f16 v[126:129], v[192:195], v[176:179], v[126:129]
	v_mfma_f32_16x16x32_f16 v[122:125], v[192:195], v[184:187], v[122:125]
	v_mfma_f32_16x16x32_f16 v[118:121], v[200:203], v[176:179], v[118:121]
	v_mfma_f32_16x16x32_f16 v[114:117], v[200:203], v[184:187], v[114:117]
	v_mfma_f32_16x16x32_f16 v[110:113], v[208:211], v[176:179], v[110:113]
	v_mfma_f32_16x16x32_f16 v[106:109], v[208:211], v[184:187], v[106:109]
	v_mfma_f32_16x16x32_f16 v[102:105], v[216:219], v[176:179], v[102:105]
	v_mfma_f32_16x16x32_f16 v[98:101], v[216:219], v[184:187], v[98:101]
	s_setprio 0
	s_barrier
	v_readfirstlane_b32 s13, v160
	v_lshl_add_u64 v[244:245], v[240:241], 0, s[20:21]
	s_mov_b32 m0, s13
	v_readfirstlane_b32 s13, v161
	ds_read_b128 v[220:223], v154
	ds_read_b128 v[224:227], v154 offset:1024
	ds_read_b128 v[228:231], v154 offset:2048
	ds_read_b128 v[232:235], v154 offset:3072
	global_load_lds_dwordx4 v[244:245], off
	v_lshl_add_u64 v[244:245], v[242:243], 0, s[20:21]
	s_mov_b32 m0, s13
	s_nop 0
	global_load_lds_dwordx4 v[244:245], off
	s_barrier
	s_waitcnt lgkmcnt(0)
	s_setprio 1
	s_waitcnt lgkmcnt(0)
	v_mfma_f32_16x16x32_f16 v[94:97], v[188:191], v[220:223], v[94:97]
	v_mfma_f32_16x16x32_f16 v[90:93], v[188:191], v[228:231], v[90:93]
	v_mfma_f32_16x16x32_f16 v[86:89], v[196:199], v[220:223], v[86:89]
	v_mfma_f32_16x16x32_f16 v[82:85], v[196:199], v[228:231], v[82:85]
	v_mfma_f32_16x16x32_f16 v[78:81], v[204:207], v[220:223], v[78:81]
	v_mfma_f32_16x16x32_f16 v[74:77], v[204:207], v[228:231], v[74:77]
	v_mfma_f32_16x16x32_f16 v[70:73], v[212:215], v[220:223], v[70:73]
	v_mfma_f32_16x16x32_f16 v[66:69], v[212:215], v[228:231], v[66:69]
	v_mfma_f32_16x16x32_f16 v[94:97], v[192:195], v[224:227], v[94:97]
	v_mfma_f32_16x16x32_f16 v[90:93], v[192:195], v[232:235], v[90:93]
	v_mfma_f32_16x16x32_f16 v[86:89], v[200:203], v[224:227], v[86:89]
	v_mfma_f32_16x16x32_f16 v[82:85], v[200:203], v[232:235], v[82:85]
	v_mfma_f32_16x16x32_f16 v[78:81], v[208:211], v[224:227], v[78:81]
	v_mfma_f32_16x16x32_f16 v[74:77], v[208:211], v[232:235], v[74:77]
	v_mfma_f32_16x16x32_f16 v[70:73], v[216:219], v[224:227], v[70:73]
	v_mfma_f32_16x16x32_f16 v[66:69], v[216:219], v[232:235], v[66:69]
	s_setprio 0
	v_readfirstlane_b32 s13, v162
	v_lshl_add_u64 v[236:237], v[236:237], 0, s[20:21]
	s_mov_b32 m0, s13
	v_readfirstlane_b32 s13, v163
	s_barrier
	ds_read_b128 v[188:191], v151 offset:49152
	ds_read_b128 v[192:195], v151 offset:50176
	ds_read_b128 v[196:199], v150 offset:49152
	ds_read_b128 v[200:203], v150 offset:50176
	ds_read_b128 v[204:207], v149 offset:49152
	ds_read_b128 v[208:211], v149 offset:50176
	ds_read_b128 v[212:215], v148 offset:49152
	ds_read_b128 v[216:219], v148 offset:50176
	global_load_lds_dwordx4 v[236:237], off
	v_lshl_add_u64 v[236:237], v[238:239], 0, s[20:21]
	s_mov_b32 m0, s13
	s_nop 0
	global_load_lds_dwordx4 v[236:237], off
	s_barrier
	s_waitcnt lgkmcnt(0)
	s_setprio 1
	s_waitcnt lgkmcnt(0)
	v_mfma_f32_16x16x32_f16 v[62:65], v[188:191], v[172:175], v[62:65]
	v_mfma_f32_16x16x32_f16 v[58:61], v[188:191], v[180:183], v[58:61]
	v_mfma_f32_16x16x32_f16 v[54:57], v[196:199], v[172:175], v[54:57]
	v_mfma_f32_16x16x32_f16 v[50:53], v[196:199], v[180:183], v[50:53]
	v_mfma_f32_16x16x32_f16 v[46:49], v[204:207], v[172:175], v[46:49]
	v_mfma_f32_16x16x32_f16 v[42:45], v[204:207], v[180:183], v[42:45]
	v_mfma_f32_16x16x32_f16 v[38:41], v[212:215], v[172:175], v[38:41]
	v_mfma_f32_16x16x32_f16 v[34:37], v[212:215], v[180:183], v[34:37]
	v_mfma_f32_16x16x32_f16 v[62:65], v[192:195], v[176:179], v[62:65]
	v_mfma_f32_16x16x32_f16 v[58:61], v[192:195], v[184:187], v[58:61]
	v_mfma_f32_16x16x32_f16 v[54:57], v[200:203], v[176:179], v[54:57]
	v_mfma_f32_16x16x32_f16 v[50:53], v[200:203], v[184:187], v[50:53]
	v_mfma_f32_16x16x32_f16 v[46:49], v[208:211], v[176:179], v[46:49]
	v_mfma_f32_16x16x32_f16 v[42:45], v[208:211], v[184:187], v[42:45]
	v_mfma_f32_16x16x32_f16 v[38:41], v[216:219], v[176:179], v[38:41]
	v_mfma_f32_16x16x32_f16 v[34:37], v[216:219], v[184:187], v[34:37]
	s_setprio 0
	s_barrier
	v_readfirstlane_b32 s13, v164
	v_lshl_add_u64 v[172:173], v[240:241], 0, s[22:23]
	s_mov_b32 m0, s13
	v_readfirstlane_b32 s13, v165
	global_load_lds_dwordx4 v[172:173], off
	v_lshl_add_u64 v[172:173], v[242:243], 0, s[22:23]
	s_mov_b32 m0, s13
	s_nop 0
	global_load_lds_dwordx4 v[172:173], off
	s_waitcnt vmcnt(6)
	s_barrier
	s_setprio 1
	v_mfma_f32_16x16x32_f16 v[30:33], v[188:191], v[220:223], v[30:33]
	v_mfma_f32_16x16x32_f16 v[26:29], v[188:191], v[228:231], v[26:29]
	v_mfma_f32_16x16x32_f16 v[22:25], v[196:199], v[220:223], v[22:25]
	v_mfma_f32_16x16x32_f16 v[18:21], v[196:199], v[228:231], v[18:21]
	v_mfma_f32_16x16x32_f16 v[14:17], v[204:207], v[220:223], v[14:17]
	v_mfma_f32_16x16x32_f16 v[10:13], v[204:207], v[228:231], v[10:13]
	v_mfma_f32_16x16x32_f16 v[6:9], v[212:215], v[220:223], v[6:9]
	v_mfma_f32_16x16x32_f16 v[2:5], v[212:215], v[228:231], v[2:5]
	v_mfma_f32_16x16x32_f16 v[30:33], v[192:195], v[224:227], v[30:33]
	v_mfma_f32_16x16x32_f16 v[26:29], v[192:195], v[232:235], v[26:29]
	v_mfma_f32_16x16x32_f16 v[22:25], v[200:203], v[224:227], v[22:25]
	v_mfma_f32_16x16x32_f16 v[18:21], v[200:203], v[232:235], v[18:21]
	v_mfma_f32_16x16x32_f16 v[14:17], v[208:211], v[224:227], v[14:17]
	v_mfma_f32_16x16x32_f16 v[10:13], v[208:211], v[232:235], v[10:13]
	v_mfma_f32_16x16x32_f16 v[6:9], v[216:219], v[224:227], v[6:9]
	v_mfma_f32_16x16x32_f16 v[2:5], v[216:219], v[232:235], v[2:5]
	s_setprio 0
	s_add_i32 s7, s7, 2
	v_lshl_add_u64 v[136:137], v[136:137], 0, s[2:3]
	v_lshl_add_u64 v[138:139], v[138:139], 0, s[2:3]
	v_lshl_add_u64 v[140:141], v[140:141], 0, s[2:3]
	s_cmp_lt_u32 s7, 12
	v_lshl_add_u64 v[142:143], v[142:143], 0, s[2:3]
	s_barrier
	s_cbranch_scc1 .LBB15_7
	s_mov_b64 s[0:1], 0x780
	v_lshl_add_u64 v[130:131], v[132:133], 0, s[0:1]
	v_add_u32_e32 v132, 0xc000, v153
	ds_read_b128 v[136:139], v167
	ds_read_b128 v[140:143], v167 offset:1024
	ds_read_b128 v[158:161], v167 offset:2048
	ds_read_b128 v[162:165], v167 offset:3072
	v_readfirstlane_b32 s2, v132
	s_mov_b32 m0, s2
	v_add_u32_e32 v132, 0xe000, v153
	global_load_lds_dwordx4 v[130:131], off
	v_lshl_add_u64 v[130:131], v[134:135], 0, s[0:1]
	v_readfirstlane_b32 s0, v132
	s_mov_b32 m0, s0
	s_nop 0
	global_load_lds_dwordx4 v[130:131], off
	ds_read_b128 v[130:133], v151
	ds_read_b128 v[168:171], v151 offset:1024
	ds_read_b128 v[172:175], v150
	ds_read_b128 v[176:179], v150 offset:1024
	ds_read_b128 v[180:183], v149
	ds_read_b128 v[184:187], v149 offset:1024
	ds_read_b128 v[188:191], v148
	ds_read_b128 v[192:195], v148 offset:1024
	s_barrier
	s_waitcnt lgkmcnt(0)
	s_setprio 1
	s_waitcnt lgkmcnt(0)
	v_mfma_f32_16x16x32_f16 v[126:129], v[130:133], v[136:139], v[126:129]
	v_mfma_f32_16x16x32_f16 v[122:125], v[130:133], v[158:161], v[122:125]
	v_mfma_f32_16x16x32_f16 v[118:121], v[172:175], v[136:139], v[118:121]
	v_mfma_f32_16x16x32_f16 v[114:117], v[172:175], v[158:161], v[114:117]
	v_mfma_f32_16x16x32_f16 v[110:113], v[180:183], v[136:139], v[110:113]
	v_mfma_f32_16x16x32_f16 v[106:109], v[180:183], v[158:161], v[106:109]
	v_mfma_f32_16x16x32_f16 v[102:105], v[188:191], v[136:139], v[102:105]
	v_mfma_f32_16x16x32_f16 v[98:101], v[188:191], v[158:161], v[98:101]
	v_mfma_f32_16x16x32_f16 v[126:129], v[168:171], v[140:143], v[126:129]
	v_mfma_f32_16x16x32_f16 v[122:125], v[168:171], v[162:165], v[122:125]
	v_mfma_f32_16x16x32_f16 v[118:121], v[176:179], v[140:143], v[118:121]
	v_mfma_f32_16x16x32_f16 v[114:117], v[176:179], v[162:165], v[114:117]
	v_mfma_f32_16x16x32_f16 v[110:113], v[184:187], v[140:143], v[110:113]
	v_mfma_f32_16x16x32_f16 v[106:109], v[184:187], v[162:165], v[106:109]
	v_mfma_f32_16x16x32_f16 v[102:105], v[192:195], v[140:143], v[102:105]
	v_mfma_f32_16x16x32_f16 v[98:101], v[192:195], v[162:165], v[98:101]
	s_setprio 0
	s_barrier
	ds_read_b128 v[196:199], v166
	ds_read_b128 v[200:203], v166 offset:1024
	ds_read_b128 v[204:207], v166 offset:2048
	ds_read_b128 v[208:211], v166 offset:3072
	s_barrier
	s_waitcnt lgkmcnt(0)
	s_setprio 1
	s_waitcnt lgkmcnt(0)
	v_mfma_f32_16x16x32_f16 v[94:97], v[130:133], v[196:199], v[94:97]
	v_mfma_f32_16x16x32_f16 v[90:93], v[130:133], v[204:207], v[90:93]
	v_mfma_f32_16x16x32_f16 v[86:89], v[172:175], v[196:199], v[86:89]
	v_mfma_f32_16x16x32_f16 v[82:85], v[172:175], v[204:207], v[82:85]
	v_mfma_f32_16x16x32_f16 v[78:81], v[180:183], v[196:199], v[78:81]
	v_mfma_f32_16x16x32_f16 v[74:77], v[180:183], v[204:207], v[74:77]
	v_mfma_f32_16x16x32_f16 v[70:73], v[188:191], v[196:199], v[70:73]
	v_mfma_f32_16x16x32_f16 v[66:69], v[188:191], v[204:207], v[66:69]
	v_mfma_f32_16x16x32_f16 v[94:97], v[168:171], v[200:203], v[94:97]
	v_mfma_f32_16x16x32_f16 v[90:93], v[168:171], v[208:211], v[90:93]
	v_mfma_f32_16x16x32_f16 v[86:89], v[176:179], v[200:203], v[86:89]
	v_mfma_f32_16x16x32_f16 v[82:85], v[176:179], v[208:211], v[82:85]
	v_mfma_f32_16x16x32_f16 v[78:81], v[184:187], v[200:203], v[78:81]
	v_mfma_f32_16x16x32_f16 v[74:77], v[184:187], v[208:211], v[74:77]
	v_mfma_f32_16x16x32_f16 v[70:73], v[192:195], v[200:203], v[70:73]
	v_mfma_f32_16x16x32_f16 v[66:69], v[192:195], v[208:211], v[66:69]
	s_setprio 0
	s_barrier
	ds_read_b128 v[130:133], v151 offset:16384
	ds_read_b128 v[166:169], v151 offset:17408
	ds_read_b128 v[170:173], v150 offset:16384
	ds_read_b128 v[174:177], v150 offset:17408
	ds_read_b128 v[178:181], v149 offset:16384
	ds_read_b128 v[182:185], v149 offset:17408
	ds_read_b128 v[186:189], v148 offset:16384
	ds_read_b128 v[190:193], v148 offset:17408
	s_waitcnt vmcnt(4)
	s_barrier
	s_waitcnt lgkmcnt(0)
	s_setprio 1
	s_waitcnt lgkmcnt(0)
	v_mfma_f32_16x16x32_f16 v[62:65], v[130:133], v[136:139], v[62:65]
	v_mfma_f32_16x16x32_f16 v[58:61], v[130:133], v[158:161], v[58:61]
	v_mfma_f32_16x16x32_f16 v[54:57], v[170:173], v[136:139], v[54:57]
	v_mfma_f32_16x16x32_f16 v[50:53], v[170:173], v[158:161], v[50:53]
	v_mfma_f32_16x16x32_f16 v[46:49], v[178:181], v[136:139], v[46:49]
	v_mfma_f32_16x16x32_f16 v[42:45], v[178:181], v[158:161], v[42:45]
	v_mfma_f32_16x16x32_f16 v[38:41], v[186:189], v[136:139], v[38:41]
	v_mfma_f32_16x16x32_f16 v[34:37], v[186:189], v[158:161], v[34:37]
	v_mfma_f32_16x16x32_f16 v[62:65], v[166:169], v[140:143], v[62:65]
	v_mfma_f32_16x16x32_f16 v[58:61], v[166:169], v[162:165], v[58:61]
	v_mfma_f32_16x16x32_f16 v[54:57], v[174:177], v[140:143], v[54:57]
	v_mfma_f32_16x16x32_f16 v[50:53], v[174:177], v[162:165], v[50:53]
	v_mfma_f32_16x16x32_f16 v[46:49], v[182:185], v[140:143], v[46:49]
	v_mfma_f32_16x16x32_f16 v[42:45], v[182:185], v[162:165], v[42:45]
	v_mfma_f32_16x16x32_f16 v[38:41], v[190:193], v[140:143], v[38:41]
	v_mfma_f32_16x16x32_f16 v[34:37], v[190:193], v[162:165], v[34:37]
	s_setprio 0
	s_setprio 1
	v_mfma_f32_16x16x32_f16 v[30:33], v[130:133], v[196:199], v[30:33]
	v_mfma_f32_16x16x32_f16 v[26:29], v[130:133], v[204:207], v[26:29]
	v_mfma_f32_16x16x32_f16 v[22:25], v[170:173], v[196:199], v[22:25]
	v_mfma_f32_16x16x32_f16 v[18:21], v[170:173], v[204:207], v[18:21]
	v_mfma_f32_16x16x32_f16 v[14:17], v[178:181], v[196:199], v[14:17]
	v_mfma_f32_16x16x32_f16 v[10:13], v[178:181], v[204:207], v[10:13]
	v_mfma_f32_16x16x32_f16 v[6:9], v[186:189], v[196:199], v[6:9]
	v_mfma_f32_16x16x32_f16 v[2:5], v[186:189], v[204:207], v[2:5]
	v_mfma_f32_16x16x32_f16 v[30:33], v[166:169], v[200:203], v[30:33]
	v_mfma_f32_16x16x32_f16 v[26:29], v[166:169], v[208:211], v[26:29]
	v_mfma_f32_16x16x32_f16 v[22:25], v[174:177], v[200:203], v[22:25]
	v_mfma_f32_16x16x32_f16 v[18:21], v[174:177], v[208:211], v[18:21]
	v_mfma_f32_16x16x32_f16 v[14:17], v[182:185], v[200:203], v[14:17]
	v_mfma_f32_16x16x32_f16 v[10:13], v[182:185], v[208:211], v[10:13]
	v_mfma_f32_16x16x32_f16 v[6:9], v[190:193], v[200:203], v[6:9]
	v_mfma_f32_16x16x32_f16 v[2:5], v[190:193], v[208:211], v[2:5]
	s_setprio 0
	s_barrier
	ds_read_b128 v[130:133], v157
	ds_read_b128 v[134:137], v157 offset:1024
	ds_read_b128 v[138:141], v157 offset:2048
	ds_read_b128 v[156:159], v157 offset:3072
	ds_read_b128 v[160:163], v151 offset:32768
	ds_read_b128 v[164:167], v151 offset:33792
	ds_read_b128 v[168:171], v150 offset:32768
	ds_read_b128 v[172:175], v150 offset:33792
	ds_read_b128 v[176:179], v149 offset:32768
	ds_read_b128 v[180:183], v149 offset:33792
	ds_read_b128 v[184:187], v148 offset:32768
	ds_read_b128 v[188:191], v148 offset:33792
	s_waitcnt vmcnt(2)
	s_barrier
	s_waitcnt lgkmcnt(0)
	s_setprio 1
	s_waitcnt lgkmcnt(0)
	v_mfma_f32_16x16x32_f16 v[126:129], v[160:163], v[130:133], v[126:129]
	v_mfma_f32_16x16x32_f16 v[122:125], v[160:163], v[138:141], v[122:125]
	v_mfma_f32_16x16x32_f16 v[118:121], v[168:171], v[130:133], v[118:121]
	v_mfma_f32_16x16x32_f16 v[114:117], v[168:171], v[138:141], v[114:117]
	v_mfma_f32_16x16x32_f16 v[110:113], v[176:179], v[130:133], v[110:113]
	v_mfma_f32_16x16x32_f16 v[106:109], v[176:179], v[138:141], v[106:109]
	v_mfma_f32_16x16x32_f16 v[102:105], v[184:187], v[130:133], v[102:105]
	v_mfma_f32_16x16x32_f16 v[98:101], v[184:187], v[138:141], v[98:101]
	v_mfma_f32_16x16x32_f16 v[126:129], v[164:167], v[134:137], v[126:129]
	v_mfma_f32_16x16x32_f16 v[122:125], v[164:167], v[156:159], v[122:125]
	v_mfma_f32_16x16x32_f16 v[118:121], v[172:175], v[134:137], v[118:121]
	v_mfma_f32_16x16x32_f16 v[114:117], v[172:175], v[156:159], v[114:117]
	v_mfma_f32_16x16x32_f16 v[110:113], v[180:183], v[134:137], v[110:113]
	v_mfma_f32_16x16x32_f16 v[106:109], v[180:183], v[156:159], v[106:109]
	v_mfma_f32_16x16x32_f16 v[102:105], v[188:191], v[134:137], v[102:105]
	v_mfma_f32_16x16x32_f16 v[98:101], v[188:191], v[156:159], v[98:101]
	s_setprio 0
	s_barrier
	ds_read_b128 v[192:195], v154
	ds_read_b128 v[196:199], v154 offset:1024
	ds_read_b128 v[200:203], v154 offset:2048
	ds_read_b128 v[152:155], v154 offset:3072
	s_waitcnt vmcnt(0)
	s_barrier
	s_waitcnt lgkmcnt(0)
	s_setprio 1
	s_waitcnt lgkmcnt(0)
	v_mfma_f32_16x16x32_f16 v[94:97], v[160:163], v[192:195], v[94:97]
	v_mfma_f32_16x16x32_f16 v[90:93], v[160:163], v[200:203], v[90:93]
	v_mfma_f32_16x16x32_f16 v[86:89], v[168:171], v[192:195], v[86:89]
	v_mfma_f32_16x16x32_f16 v[82:85], v[168:171], v[200:203], v[82:85]
	v_mfma_f32_16x16x32_f16 v[78:81], v[176:179], v[192:195], v[78:81]
	v_mfma_f32_16x16x32_f16 v[74:77], v[176:179], v[200:203], v[74:77]
	v_mfma_f32_16x16x32_f16 v[70:73], v[184:187], v[192:195], v[70:73]
	v_mfma_f32_16x16x32_f16 v[66:69], v[184:187], v[200:203], v[66:69]
	v_mfma_f32_16x16x32_f16 v[94:97], v[164:167], v[196:199], v[94:97]
	v_mfma_f32_16x16x32_f16 v[90:93], v[164:167], v[152:155], v[90:93]
	v_mfma_f32_16x16x32_f16 v[86:89], v[172:175], v[196:199], v[86:89]
	v_mfma_f32_16x16x32_f16 v[82:85], v[172:175], v[152:155], v[82:85]
	v_mfma_f32_16x16x32_f16 v[78:81], v[180:183], v[196:199], v[78:81]
	v_mfma_f32_16x16x32_f16 v[74:77], v[180:183], v[152:155], v[74:77]
	v_mfma_f32_16x16x32_f16 v[70:73], v[188:191], v[196:199], v[70:73]
	v_mfma_f32_16x16x32_f16 v[66:69], v[188:191], v[152:155], v[66:69]
	s_setprio 0
	s_barrier
	ds_read_b128 v[160:163], v151 offset:49152
	ds_read_b128 v[164:167], v151 offset:50176
	ds_read_b128 v[168:171], v150 offset:49152
	ds_read_b128 v[172:175], v150 offset:50176
	ds_read_b128 v[176:179], v149 offset:49152
	ds_read_b128 v[180:183], v149 offset:50176
	ds_read_b128 v[184:187], v148 offset:49152
	ds_read_b128 v[148:151], v148 offset:50176
	s_barrier
	s_waitcnt lgkmcnt(0)
	s_setprio 1
	s_waitcnt lgkmcnt(0)
	v_mfma_f32_16x16x32_f16 v[62:65], v[160:163], v[130:133], v[62:65]
	v_mfma_f32_16x16x32_f16 v[58:61], v[160:163], v[138:141], v[58:61]
	v_mfma_f32_16x16x32_f16 v[54:57], v[168:171], v[130:133], v[54:57]
	v_mfma_f32_16x16x32_f16 v[50:53], v[168:171], v[138:141], v[50:53]
	v_mfma_f32_16x16x32_f16 v[46:49], v[176:179], v[130:133], v[46:49]
	v_mfma_f32_16x16x32_f16 v[42:45], v[176:179], v[138:141], v[42:45]
	v_mfma_f32_16x16x32_f16 v[38:41], v[184:187], v[130:133], v[38:41]
	v_mfma_f32_16x16x32_f16 v[34:37], v[184:187], v[138:141], v[34:37]
	v_mfma_f32_16x16x32_f16 v[62:65], v[164:167], v[134:137], v[62:65]
	v_mfma_f32_16x16x32_f16 v[58:61], v[164:167], v[156:159], v[58:61]
	v_mfma_f32_16x16x32_f16 v[54:57], v[172:175], v[134:137], v[54:57]
	v_mfma_f32_16x16x32_f16 v[50:53], v[172:175], v[156:159], v[50:53]
	v_mfma_f32_16x16x32_f16 v[46:49], v[180:183], v[134:137], v[46:49]
	v_mfma_f32_16x16x32_f16 v[42:45], v[180:183], v[156:159], v[42:45]
	v_mfma_f32_16x16x32_f16 v[38:41], v[148:151], v[134:137], v[38:41]
	v_mfma_f32_16x16x32_f16 v[34:37], v[148:151], v[156:159], v[34:37]
	s_setprio 0
	s_setprio 1
	v_mfma_f32_16x16x32_f16 v[30:33], v[160:163], v[192:195], v[30:33]
	v_mfma_f32_16x16x32_f16 v[26:29], v[160:163], v[200:203], v[26:29]
	v_mfma_f32_16x16x32_f16 v[22:25], v[168:171], v[192:195], v[22:25]
	v_mfma_f32_16x16x32_f16 v[18:21], v[168:171], v[200:203], v[18:21]
	v_mfma_f32_16x16x32_f16 v[14:17], v[176:179], v[192:195], v[14:17]
	v_mfma_f32_16x16x32_f16 v[10:13], v[176:179], v[200:203], v[10:13]
	v_mfma_f32_16x16x32_f16 v[6:9], v[184:187], v[192:195], v[6:9]
	v_mfma_f32_16x16x32_f16 v[2:5], v[184:187], v[200:203], v[2:5]
	v_mfma_f32_16x16x32_f16 v[30:33], v[164:167], v[196:199], v[30:33]
	v_mfma_f32_16x16x32_f16 v[26:29], v[164:167], v[152:155], v[26:29]
	v_mfma_f32_16x16x32_f16 v[22:25], v[172:175], v[196:199], v[22:25]
	v_mfma_f32_16x16x32_f16 v[18:21], v[172:175], v[152:155], v[18:21]
	v_mfma_f32_16x16x32_f16 v[14:17], v[180:183], v[196:199], v[14:17]
	v_mfma_f32_16x16x32_f16 v[10:13], v[180:183], v[152:155], v[10:13]
	v_mfma_f32_16x16x32_f16 v[6:9], v[148:151], v[196:199], v[6:9]
	v_mfma_f32_16x16x32_f16 v[2:5], v[148:151], v[152:155], v[2:5]
	s_setprio 0
	s_branch .Lg8_merge
.Lg8b_entry:
	s_and_b64 s[12:13], s[4:5], exec
	global_load_lds_dwordx4 v[2:3], off
	s_mov_b32 m0, s7
	s_cselect_b32 s7, s11, s9
	s_cselect_b32 s23, s10, s8
	s_lshl_b32 s12, s14, 8
	s_ashr_i32 s13, s12, 31
	s_lshl_b64 s[18:19], s[12:13], 11
	s_add_u32 s8, s23, s18
	s_addc_u32 s9, s7, s19
	v_add_u32_e32 v153, 0, v1
	v_lshl_add_u64 v[4:5], v[4:5], 0, v[20:21]
	v_lshl_add_u64 v[8:9], s[8:9], 0, v[130:131]
	v_readfirstlane_b32 s8, v153
	v_add_u32_e32 v155, 0x2000, v153
	global_load_lds_dwordx4 v[4:5], off
	v_lshl_add_u64 v[6:7], v[8:9], 0, v[18:19]
	s_mov_b32 m0, s8
	v_readfirstlane_b32 s8, v155
	global_load_lds_dwordx4 v[6:7], off
	s_mov_b32 m0, s8
	s_or_b32 s8, s6, 0x80
	s_ashr_i32 s9, s8, 31
	s_lshl_b64 s[8:9], s[8:9], 11
	s_add_u32 s8, s21, s8
	s_addc_u32 s9, s20, s9
	s_add_i32 s13, 0, 0x14000
	v_add_u32_e32 v156, s13, v1
	v_lshl_add_u64 v[8:9], v[8:9], 0, v[20:21]
	v_lshl_add_u64 v[12:13], s[8:9], 0, v[130:131]
	v_readfirstlane_b32 s8, v156
	v_add_u32_e32 v22, s13, v17
	global_load_lds_dwordx4 v[8:9], off
	v_lshl_add_u64 v[10:11], v[12:13], 0, v[18:19]
	s_mov_b32 m0, s8
	v_readfirstlane_b32 s8, v22
	global_load_lds_dwordx4 v[10:11], off
	s_mov_b32 m0, s8
	s_or_b32 s8, s12, 0x80
	s_ashr_i32 s9, s8, 31
	s_lshl_b64 s[8:9], s[8:9], 11
	s_add_u32 s8, s23, s8
	s_addc_u32 s9, s7, s9
	v_add_u32_e32 v158, 0x4000, v153
	v_lshl_add_u64 v[12:13], v[12:13], 0, v[20:21]
	v_lshl_add_u64 v[22:23], s[8:9], 0, v[130:131]
	v_readfirstlane_b32 s8, v158
	v_add_u32_e32 v159, 0x6000, v153
	global_load_lds_dwordx4 v[12:13], off
	v_lshl_add_u64 v[132:133], v[22:23], 0, v[18:19]
	s_mov_b32 m0, s8
	v_readfirstlane_b32 s8, v159
	global_load_lds_dwordx4 v[132:133], off
	v_lshl_add_u64 v[134:135], v[22:23], 0, v[20:21]
	s_mov_b32 m0, s8
	v_cmp_eq_u32_e32 vcc, 1, v145
	global_load_lds_dwordx4 v[134:135], off
	s_load_dwordx2 s[16:17], s[0:1], 0x30
	s_load_dwordx2 s[14:15], s[0:1], 0x40
	s_and_saveexec_b64 s[8:9], vcc
	s_cbranch_execz .Lg8b_6
	s_barrier

.Lg8b_7:
	ds_read_b128 v[172:175], v167
	ds_read_b128 v[176:179], v167 offset:1024
	ds_read_b128 v[180:183], v167 offset:2048
	ds_read_b128 v[184:187], v167 offset:3072
	v_lshl_add_u64 v[236:237], v[138:139], 0, v[130:131]
	v_readfirstlane_b32 s13, v168
	v_lshl_add_u64 v[188:189], v[236:237], 0, s[0:1]
	s_mov_b32 m0, s13
	v_lshl_add_u64 v[238:239], v[136:137], 0, v[130:131]
	v_readfirstlane_b32 s13, v169
	global_load_lds_dwordx4 v[188:189], off
	v_lshl_add_u64 v[188:189], v[238:239], 0, s[0:1]
	s_mov_b32 m0, s13
	s_nop 0
	global_load_lds_dwordx4 v[188:189], off
	ds_read_b128 v[188:191], v151
	ds_read_b128 v[192:195], v151 offset:1024
	ds_read_b128 v[196:199], v150
	ds_read_b128 v[200:203], v150 offset:1024
	ds_read_b128 v[204:207], v149
	ds_read_b128 v[208:211], v149 offset:1024
	ds_read_b128 v[212:215], v148
	ds_read_b128 v[216:219], v148 offset:1024
	s_waitcnt lgkmcnt(8)
	s_barrier
	s_waitcnt lgkmcnt(0)
	s_setprio 2
	s_waitcnt lgkmcnt(0)
	v_mfma_f32_16x16x32_f16 v[126:129], v[188:191], v[172:175], v[126:129]
	v_mfma_f32_16x16x32_f16 v[122:125], v[188:191], v[180:183], v[122:125]
	v_mfma_f32_16x16x32_f16 v[118:121], v[196:199], v[172:175], v[118:121]
	v_mfma_f32_16x16x32_f16 v[114:117], v[196:199], v[180:183], v[114:117]
	v_mfma_f32_16x16x32_f16 v[110:113], v[204:207], v[172:175], v[110:113]
	v_mfma_f32_16x16x32_f16 v[106:109], v[204:207], v[180:183], v[106:109]
	v_mfma_f32_16x16x32_f16 v[102:105], v[212:215], v[172:175], v[102:105]
	v_mfma_f32_16x16x32_f16 v[98:101], v[212:215], v[180:183], v[98:101]
	v_mfma_f32_16x16x32_f16 v[126:129], v[192:195], v[176:179], v[126:129]
	v_mfma_f32_16x16x32_f16 v[122:125], v[192:195], v[184:187], v[122:125]
	v_mfma_f32_16x16x32_f16 v[118:121], v[200:203], v[176:179], v[118:121]
	v_mfma_f32_16x16x32_f16 v[114:117], v[200:203], v[184:187], v[114:117]
	v_mfma_f32_16x16x32_f16 v[110:113], v[208:211], v[176:179], v[110:113]
	v_mfma_f32_16x16x32_f16 v[106:109], v[208:211], v[184:187], v[106:109]
	v_mfma_f32_16x16x32_f16 v[102:105], v[216:219], v[176:179], v[102:105]
	v_mfma_f32_16x16x32_f16 v[98:101], v[216:219], v[184:187], v[98:101]
	s_setprio 1
	s_barrier
	v_lshl_add_u64 v[240:241], v[142:143], 0, v[130:131]
	v_readfirstlane_b32 s13, v152
	v_lshl_add_u64 v[242:243], v[240:241], 0, s[2:3]
	s_mov_b32 m0, s13
	ds_read_b128 v[220:223], v166
	ds_read_b128 v[224:227], v166 offset:1024
	ds_read_b128 v[228:231], v166 offset:2048
	ds_read_b128 v[232:235], v166 offset:3072
	global_load_lds_dwordx4 v[242:243], off
	v_lshl_add_u64 v[242:243], v[140:141], 0, v[130:131]
	v_readfirstlane_b32 s13, v170
	v_lshl_add_u64 v[244:245], v[242:243], 0, s[2:3]
	s_mov_b32 m0, s13
	s_nop 0
	global_load_lds_dwordx4 v[244:245], off
	s_barrier
	s_waitcnt lgkmcnt(0)
	s_setprio 2
	s_waitcnt lgkmcnt(0)
	v_mfma_f32_16x16x32_f16 v[94:97], v[188:191], v[220:223], v[94:97]
	v_mfma_f32_16x16x32_f16 v[90:93], v[188:191], v[228:231], v[90:93]
	v_mfma_f32_16x16x32_f16 v[86:89], v[196:199], v[220:223], v[86:89]
	v_mfma_f32_16x16x32_f16 v[82:85], v[196:199], v[228:231], v[82:85]
	v_mfma_f32_16x16x32_f16 v[78:81], v[204:207], v[220:223], v[78:81]
	v_mfma_f32_16x16x32_f16 v[74:77], v[204:207], v[228:231], v[74:77]
	v_mfma_f32_16x16x32_f16 v[70:73], v[212:215], v[220:223], v[70:73]
	v_mfma_f32_16x16x32_f16 v[66:69], v[212:215], v[228:231], v[66:69]
	v_mfma_f32_16x16x32_f16 v[94:97], v[192:195], v[224:227], v[94:97]
	v_mfma_f32_16x16x32_f16 v[90:93], v[192:195], v[232:235], v[90:93]
	v_mfma_f32_16x16x32_f16 v[86:89], v[200:203], v[224:227], v[86:89]
	v_mfma_f32_16x16x32_f16 v[82:85], v[200:203], v[232:235], v[82:85]
	v_mfma_f32_16x16x32_f16 v[78:81], v[208:211], v[224:227], v[78:81]
	v_mfma_f32_16x16x32_f16 v[74:77], v[208:211], v[232:235], v[74:77]
	v_mfma_f32_16x16x32_f16 v[70:73], v[216:219], v[224:227], v[70:73]
	v_mfma_f32_16x16x32_f16 v[66:69], v[216:219], v[232:235], v[66:69]
	s_setprio 1
	v_readfirstlane_b32 s13, v153
	v_lshl_add_u64 v[244:245], v[236:237], 0, s[2:3]
	s_mov_b32 m0, s13
	v_readfirstlane_b32 s13, v155
	s_barrier
	ds_read_b128 v[188:191], v151 offset:16384
	ds_read_b128 v[192:195], v151 offset:17408
	ds_read_b128 v[196:199], v150 offset:16384
	ds_read_b128 v[200:203], v150 offset:17408
	ds_read_b128 v[204:207], v149 offset:16384
	ds_read_b128 v[208:211], v149 offset:17408
	ds_read_b128 v[212:215], v148 offset:16384
	ds_read_b128 v[216:219], v148 offset:17408
	global_load_lds_dwordx4 v[244:245], off
	v_lshl_add_u64 v[244:245], v[238:239], 0, s[2:3]
	s_mov_b32 m0, s13
	s_nop 0
	global_load_lds_dwordx4 v[244:245], off
	s_barrier
	s_waitcnt lgkmcnt(0)
	s_setprio 2
	s_waitcnt lgkmcnt(0)
	v_mfma_f32_16x16x32_f16 v[62:65], v[188:191], v[172:175], v[62:65]
	v_mfma_f32_16x16x32_f16 v[58:61], v[188:191], v[180:183], v[58:61]
	v_mfma_f32_16x16x32_f16 v[54:57], v[196:199], v[172:175], v[54:57]
	v_mfma_f32_16x16x32_f16 v[50:53], v[196:199], v[180:183], v[50:53]
	v_mfma_f32_16x16x32_f16 v[46:49], v[204:207], v[172:175], v[46:49]
	v_mfma_f32_16x16x32_f16 v[42:45], v[204:207], v[180:183], v[42:45]
	v_mfma_f32_16x16x32_f16 v[38:41], v[212:215], v[172:175], v[38:41]
	v_mfma_f32_16x16x32_f16 v[34:37], v[212:215], v[180:183], v[34:37]
	v_mfma_f32_16x16x32_f16 v[62:65], v[192:195], v[176:179], v[62:65]
	v_mfma_f32_16x16x32_f16 v[58:61], v[192:195], v[184:187], v[58:61]
	v_mfma_f32_16x16x32_f16 v[54:57], v[200:203], v[176:179], v[54:57]
	v_mfma_f32_16x16x32_f16 v[50:53], v[200:203], v[184:187], v[50:53]
	v_mfma_f32_16x16x32_f16 v[46:49], v[208:211], v[176:179], v[46:49]
	v_mfma_f32_16x16x32_f16 v[42:45], v[208:211], v[184:187], v[42:45]
	v_mfma_f32_16x16x32_f16 v[38:41], v[216:219], v[176:179], v[38:41]
	v_mfma_f32_16x16x32_f16 v[34:37], v[216:219], v[184:187], v[34:37]
	s_setprio 1
	s_barrier
	v_readfirstlane_b32 s13, v156
	v_lshl_add_u64 v[172:173], v[240:241], 0, s[18:19]
	s_mov_b32 m0, s13
	v_readfirstlane_b32 s13, v171
	global_load_lds_dwordx4 v[172:173], off
	v_lshl_add_u64 v[172:173], v[242:243], 0, s[18:19]
	s_mov_b32 m0, s13
	s_nop 0
	global_load_lds_dwordx4 v[172:173], off
	s_waitcnt vmcnt(6)
	s_barrier
	s_setprio 2
	v_mfma_f32_16x16x32_f16 v[30:33], v[188:191], v[220:223], v[30:33]
	v_mfma_f32_16x16x32_f16 v[26:29], v[188:191], v[228:231], v[26:29]
	v_mfma_f32_16x16x32_f16 v[22:25], v[196:199], v[220:223], v[22:25]
	v_mfma_f32_16x16x32_f16 v[18:21], v[196:199], v[228:231], v[18:21]
	v_mfma_f32_16x16x32_f16 v[14:17], v[204:207], v[220:223], v[14:17]
	v_mfma_f32_16x16x32_f16 v[10:13], v[204:207], v[228:231], v[10:13]
	v_mfma_f32_16x16x32_f16 v[6:9], v[212:215], v[220:223], v[6:9]
	v_mfma_f32_16x16x32_f16 v[2:5], v[212:215], v[228:231], v[2:5]
	v_mfma_f32_16x16x32_f16 v[30:33], v[192:195], v[224:227], v[30:33]
	v_mfma_f32_16x16x32_f16 v[26:29], v[192:195], v[232:235], v[26:29]
	v_mfma_f32_16x16x32_f16 v[22:25], v[200:203], v[224:227], v[22:25]
	v_mfma_f32_16x16x32_f16 v[18:21], v[200:203], v[232:235], v[18:21]
	v_mfma_f32_16x16x32_f16 v[14:17], v[208:211], v[224:227], v[14:17]
	v_mfma_f32_16x16x32_f16 v[10:13], v[208:211], v[232:235], v[10:13]
	v_mfma_f32_16x16x32_f16 v[6:9], v[216:219], v[224:227], v[6:9]
	v_mfma_f32_16x16x32_f16 v[2:5], v[216:219], v[232:235], v[2:5]
	s_setprio 1
	s_barrier
	ds_read_b128 v[172:175], v157
	ds_read_b128 v[176:179], v157 offset:1024
	ds_read_b128 v[180:183], v157 offset:2048
	ds_read_b128 v[184:187], v157 offset:3072
	v_readfirstlane_b32 s13, v158
	v_lshl_add_u64 v[220:221], v[236:237], 0, s[18:19]
	s_mov_b32 m0, s13
	v_readfirstlane_b32 s13, v159
	ds_read_b128 v[188:191], v151 offset:32768
	ds_read_b128 v[192:195], v151 offset:33792
	ds_read_b128 v[196:199], v150 offset:32768
	ds_read_b128 v[200:203], v150 offset:33792
	ds_read_b128 v[204:207], v149 offset:32768
	ds_read_b128 v[208:211], v149 offset:33792
	ds_read_b128 v[212:215], v148 offset:32768
	ds_read_b128 v[216:219], v148 offset:33792
	global_load_lds_dwordx4 v[220:221], off
	v_lshl_add_u64 v[220:221], v[238:239], 0, s[18:19]
	s_mov_b32 m0, s13
	s_nop 0
	global_load_lds_dwordx4 v[220:221], off
	s_waitcnt lgkmcnt(8)
	s_barrier
	s_waitcnt lgkmcnt(0)
	s_setprio 2
	s_waitcnt lgkmcnt(0)
	v_mfma_f32_16x16x32_f16 v[126:129], v[188:191], v[172:175], v[126:129]
	v_mfma_f32_16x16x32_f16 v[122:125], v[188:191], v[180:183], v[122:125]
	v_mfma_f32_16x16x32_f16 v[118:121], v[196:199], v[172:175], v[118:121]
	v_mfma_f32_16x16x32_f16 v[114:117], v[196:199], v[180:183], v[114:117]
	v_mfma_f32_16x16x32_f16 v[110:113], v[204:207], v[172:175], v[110:113]
	v_mfma_f32_16x16x32_f16 v[106:109], v[204:207], v[180:183], v[106:109]
	v_mfma_f32_16x16x32_f16 v[102:105], v[212:215], v[172:175], v[102:105]
	v_mfma_f32_16x16x32_f16 v[98:101], v[212:215], v[180:183], v[98:101]
	v_mfma_f32_16x16x32_f16 v[126:129], v[192:195], v[176:179], v[126:129]
	v_mfma_f32_16x16x32_f16 v[122:125], v[192:195], v[184:187], v[122:125]
	v_mfma_f32_16x16x32_f16 v[118:121], v[200:203], v[176:179], v[118:121]
	v_mfma_f32_16x16x32_f16 v[114:117], v[200:203], v[184:187], v[114:117]
	v_mfma_f32_16x16x32_f16 v[110:113], v[208:211], v[176:179], v[110:113]
	v_mfma_f32_16x16x32_f16 v[106:109], v[208:211], v[184:187], v[106:109]
	v_mfma_f32_16x16x32_f16 v[102:105], v[216:219], v[176:179], v[102:105]
	v_mfma_f32_16x16x32_f16 v[98:101], v[216:219], v[184:187], v[98:101]
	s_setprio 1
	s_barrier
	v_readfirstlane_b32 s13, v160
	v_lshl_add_u64 v[244:245], v[240:241], 0, s[20:21]
	s_mov_b32 m0, s13
	v_readfirstlane_b32 s13, v161
	ds_read_b128 v[220:223], v154
	ds_read_b128 v[224:227], v154 offset:1024
	ds_read_b128 v[228:231], v154 offset:2048
	ds_read_b128 v[232:235], v154 offset:3072
	global_load_lds_dwordx4 v[244:245], off
	v_lshl_add_u64 v[244:245], v[242:243], 0, s[20:21]
	s_mov_b32 m0, s13
	s_nop 0
	global_load_lds_dwordx4 v[244:245], off
	s_barrier
	s_waitcnt lgkmcnt(0)
	s_setprio 2
	s_waitcnt lgkmcnt(0)
	v_mfma_f32_16x16x32_f16 v[94:97], v[188:191], v[220:223], v[94:97]
	v_mfma_f32_16x16x32_f16 v[90:93], v[188:191], v[228:231], v[90:93]
	v_mfma_f32_16x16x32_f16 v[86:89], v[196:199], v[220:223], v[86:89]
	v_mfma_f32_16x16x32_f16 v[82:85], v[196:199], v[228:231], v[82:85]
	v_mfma_f32_16x16x32_f16 v[78:81], v[204:207], v[220:223], v[78:81]
	v_mfma_f32_16x16x32_f16 v[74:77], v[204:207], v[228:231], v[74:77]
	v_mfma_f32_16x16x32_f16 v[70:73], v[212:215], v[220:223], v[70:73]
	v_mfma_f32_16x16x32_f16 v[66:69], v[212:215], v[228:231], v[66:69]
	v_mfma_f32_16x16x32_f16 v[94:97], v[192:195], v[224:227], v[94:97]
	v_mfma_f32_16x16x32_f16 v[90:93], v[192:195], v[232:235], v[90:93]
	v_mfma_f32_16x16x32_f16 v[86:89], v[200:203], v[224:227], v[86:89]
	v_mfma_f32_16x16x32_f16 v[82:85], v[200:203], v[232:235], v[82:85]
	v_mfma_f32_16x16x32_f16 v[78:81], v[208:211], v[224:227], v[78:81]
	v_mfma_f32_16x16x32_f16 v[74:77], v[208:211], v[232:235], v[74:77]
	v_mfma_f32_16x16x32_f16 v[70:73], v[216:219], v[224:227], v[70:73]
	v_mfma_f32_16x16x32_f16 v[66:69], v[216:219], v[232:235], v[66:69]
	s_setprio 1
	v_readfirstlane_b32 s13, v162
	v_lshl_add_u64 v[236:237], v[236:237], 0, s[20:21]
	s_mov_b32 m0, s13
	v_readfirstlane_b32 s13, v163
	s_barrier
	ds_read_b128 v[188:191], v151 offset:49152
	ds_read_b128 v[192:195], v151 offset:50176
	ds_read_b128 v[196:199], v150 offset:49152
	ds_read_b128 v[200:203], v150 offset:50176
	ds_read_b128 v[204:207], v149 offset:49152
	ds_read_b128 v[208:211], v149 offset:50176
	ds_read_b128 v[212:215], v148 offset:49152
	ds_read_b128 v[216:219], v148 offset:50176
	global_load_lds_dwordx4 v[236:237], off
	v_lshl_add_u64 v[236:237], v[238:239], 0, s[20:21]
	s_mov_b32 m0, s13
	s_nop 0
	global_load_lds_dwordx4 v[236:237], off
	s_barrier
	s_waitcnt lgkmcnt(0)
	s_setprio 2
	s_waitcnt lgkmcnt(0)
	v_mfma_f32_16x16x32_f16 v[62:65], v[188:191], v[172:175], v[62:65]
	v_mfma_f32_16x16x32_f16 v[58:61], v[188:191], v[180:183], v[58:61]
	v_mfma_f32_16x16x32_f16 v[54:57], v[196:199], v[172:175], v[54:57]
	v_mfma_f32_16x16x32_f16 v[50:53], v[196:199], v[180:183], v[50:53]
	v_mfma_f32_16x16x32_f16 v[46:49], v[204:207], v[172:175], v[46:49]
	v_mfma_f32_16x16x32_f16 v[42:45], v[204:207], v[180:183], v[42:45]
	v_mfma_f32_16x16x32_f16 v[38:41], v[212:215], v[172:175], v[38:41]
	v_mfma_f32_16x16x32_f16 v[34:37], v[212:215], v[180:183], v[34:37]
	v_mfma_f32_16x16x32_f16 v[62:65], v[192:195], v[176:179], v[62:65]
	v_mfma_f32_16x16x32_f16 v[58:61], v[192:195], v[184:187], v[58:61]
	v_mfma_f32_16x16x32_f16 v[54:57], v[200:203], v[176:179], v[54:57]
	v_mfma_f32_16x16x32_f16 v[50:53], v[200:203], v[184:187], v[50:53]
	v_mfma_f32_16x16x32_f16 v[46:49], v[208:211], v[176:179], v[46:49]
	v_mfma_f32_16x16x32_f16 v[42:45], v[208:211], v[184:187], v[42:45]
	v_mfma_f32_16x16x32_f16 v[38:41], v[216:219], v[176:179], v[38:41]
	v_mfma_f32_16x16x32_f16 v[34:37], v[216:219], v[184:187], v[34:37]
	s_setprio 1
	s_barrier
	v_readfirstlane_b32 s13, v164
	v_lshl_add_u64 v[172:173], v[240:241], 0, s[22:23]
	s_mov_b32 m0, s13
	v_readfirstlane_b32 s13, v165
	global_load_lds_dwordx4 v[172:173], off
	v_lshl_add_u64 v[172:173], v[242:243], 0, s[22:23]
	s_mov_b32 m0, s13
	s_nop 0
	global_load_lds_dwordx4 v[172:173], off
	s_waitcnt vmcnt(6)
	s_barrier
	s_setprio 2
	v_mfma_f32_16x16x32_f16 v[30:33], v[188:191], v[220:223], v[30:33]
	v_mfma_f32_16x16x32_f16 v[26:29], v[188:191], v[228:231], v[26:29]
	v_mfma_f32_16x16x32_f16 v[22:25], v[196:199], v[220:223], v[22:25]
	v_mfma_f32_16x16x32_f16 v[18:21], v[196:199], v[228:231], v[18:21]
	v_mfma_f32_16x16x32_f16 v[14:17], v[204:207], v[220:223], v[14:17]
	v_mfma_f32_16x16x32_f16 v[10:13], v[204:207], v[228:231], v[10:13]
	v_mfma_f32_16x16x32_f16 v[6:9], v[212:215], v[220:223], v[6:9]
	v_mfma_f32_16x16x32_f16 v[2:5], v[212:215], v[228:231], v[2:5]
	v_mfma_f32_16x16x32_f16 v[30:33], v[192:195], v[224:227], v[30:33]
	v_mfma_f32_16x16x32_f16 v[26:29], v[192:195], v[232:235], v[26:29]
	v_mfma_f32_16x16x32_f16 v[22:25], v[200:203], v[224:227], v[22:25]
	v_mfma_f32_16x16x32_f16 v[18:21], v[200:203], v[232:235], v[18:21]
	v_mfma_f32_16x16x32_f16 v[14:17], v[208:211], v[224:227], v[14:17]
	v_mfma_f32_16x16x32_f16 v[10:13], v[208:211], v[232:235], v[10:13]
	v_mfma_f32_16x16x32_f16 v[6:9], v[216:219], v[224:227], v[6:9]
	v_mfma_f32_16x16x32_f16 v[2:5], v[216:219], v[232:235], v[2:5]
	s_setprio 1
	s_add_i32 s7, s7, 2
	v_lshl_add_u64 v[136:137], v[136:137], 0, s[2:3]
	v_lshl_add_u64 v[138:139], v[138:139], 0, s[2:3]
	v_lshl_add_u64 v[140:141], v[140:141], 0, s[2:3]
	s_cmp_lt_u32 s7, 12
	v_lshl_add_u64 v[142:143], v[142:143], 0, s[2:3]
	s_barrier
	s_cbranch_scc1 .Lg8b_7
	s_mov_b64 s[0:1], 0x780
	v_lshl_add_u64 v[130:131], v[132:133], 0, s[0:1]
	v_add_u32_e32 v132, 0xc000, v153
	ds_read_b128 v[136:139], v167
	ds_read_b128 v[140:143], v167 offset:1024
	ds_read_b128 v[158:161], v167 offset:2048
	ds_read_b128 v[162:165], v167 offset:3072
	v_readfirstlane_b32 s2, v132
	s_mov_b32 m0, s2
	v_add_u32_e32 v132, 0xe000, v153
	global_load_lds_dwordx4 v[130:131], off
	v_lshl_add_u64 v[130:131], v[134:135], 0, s[0:1]
	v_readfirstlane_b32 s0, v132
	s_mov_b32 m0, s0
	s_nop 0
	global_load_lds_dwordx4 v[130:131], off
	ds_read_b128 v[130:133], v151
	ds_read_b128 v[168:171], v151 offset:1024
	ds_read_b128 v[172:175], v150
	ds_read_b128 v[176:179], v150 offset:1024
	ds_read_b128 v[180:183], v149
	ds_read_b128 v[184:187], v149 offset:1024
	ds_read_b128 v[188:191], v148
	ds_read_b128 v[192:195], v148 offset:1024
	s_barrier
	s_waitcnt lgkmcnt(0)
	s_setprio 2
	s_waitcnt lgkmcnt(0)
	v_mfma_f32_16x16x32_f16 v[126:129], v[130:133], v[136:139], v[126:129]
	v_mfma_f32_16x16x32_f16 v[122:125], v[130:133], v[158:161], v[122:125]
	v_mfma_f32_16x16x32_f16 v[118:121], v[172:175], v[136:139], v[118:121]
	v_mfma_f32_16x16x32_f16 v[114:117], v[172:175], v[158:161], v[114:117]
	v_mfma_f32_16x16x32_f16 v[110:113], v[180:183], v[136:139], v[110:113]
	v_mfma_f32_16x16x32_f16 v[106:109], v[180:183], v[158:161], v[106:109]
	v_mfma_f32_16x16x32_f16 v[102:105], v[188:191], v[136:139], v[102:105]
	v_mfma_f32_16x16x32_f16 v[98:101], v[188:191], v[158:161], v[98:101]
	v_mfma_f32_16x16x32_f16 v[126:129], v[168:171], v[140:143], v[126:129]
	v_mfma_f32_16x16x32_f16 v[122:125], v[168:171], v[162:165], v[122:125]
	v_mfma_f32_16x16x32_f16 v[118:121], v[176:179], v[140:143], v[118:121]
	v_mfma_f32_16x16x32_f16 v[114:117], v[176:179], v[162:165], v[114:117]
	v_mfma_f32_16x16x32_f16 v[110:113], v[184:187], v[140:143], v[110:113]
	v_mfma_f32_16x16x32_f16 v[106:109], v[184:187], v[162:165], v[106:109]
	v_mfma_f32_16x16x32_f16 v[102:105], v[192:195], v[140:143], v[102:105]
	v_mfma_f32_16x16x32_f16 v[98:101], v[192:195], v[162:165], v[98:101]
	s_setprio 1
	s_barrier
	ds_read_b128 v[196:199], v166
	ds_read_b128 v[200:203], v166 offset:1024
	ds_read_b128 v[204:207], v166 offset:2048
	ds_read_b128 v[208:211], v166 offset:3072
	s_barrier
	s_waitcnt lgkmcnt(0)
	s_setprio 2
	s_waitcnt lgkmcnt(0)
	v_mfma_f32_16x16x32_f16 v[94:97], v[130:133], v[196:199], v[94:97]
	v_mfma_f32_16x16x32_f16 v[90:93], v[130:133], v[204:207], v[90:93]
	v_mfma_f32_16x16x32_f16 v[86:89], v[172:175], v[196:199], v[86:89]
	v_mfma_f32_16x16x32_f16 v[82:85], v[172:175], v[204:207], v[82:85]
	v_mfma_f32_16x16x32_f16 v[78:81], v[180:183], v[196:199], v[78:81]
	v_mfma_f32_16x16x32_f16 v[74:77], v[180:183], v[204:207], v[74:77]
	v_mfma_f32_16x16x32_f16 v[70:73], v[188:191], v[196:199], v[70:73]
	v_mfma_f32_16x16x32_f16 v[66:69], v[188:191], v[204:207], v[66:69]
	v_mfma_f32_16x16x32_f16 v[94:97], v[168:171], v[200:203], v[94:97]
	v_mfma_f32_16x16x32_f16 v[90:93], v[168:171], v[208:211], v[90:93]
	v_mfma_f32_16x16x32_f16 v[86:89], v[176:179], v[200:203], v[86:89]
	v_mfma_f32_16x16x32_f16 v[82:85], v[176:179], v[208:211], v[82:85]
	v_mfma_f32_16x16x32_f16 v[78:81], v[184:187], v[200:203], v[78:81]
	v_mfma_f32_16x16x32_f16 v[74:77], v[184:187], v[208:211], v[74:77]
	v_mfma_f32_16x16x32_f16 v[70:73], v[192:195], v[200:203], v[70:73]
	v_mfma_f32_16x16x32_f16 v[66:69], v[192:195], v[208:211], v[66:69]
	s_setprio 1
	s_barrier
	ds_read_b128 v[130:133], v151 offset:16384
	ds_read_b128 v[166:169], v151 offset:17408
	ds_read_b128 v[170:173], v150 offset:16384
	ds_read_b128 v[174:177], v150 offset:17408
	ds_read_b128 v[178:181], v149 offset:16384
	ds_read_b128 v[182:185], v149 offset:17408
	ds_read_b128 v[186:189], v148 offset:16384
	ds_read_b128 v[190:193], v148 offset:17408
	s_waitcnt vmcnt(4)
	s_barrier
	s_waitcnt lgkmcnt(0)
	s_setprio 2
	s_waitcnt lgkmcnt(0)
	v_mfma_f32_16x16x32_f16 v[62:65], v[130:133], v[136:139], v[62:65]
	v_mfma_f32_16x16x32_f16 v[58:61], v[130:133], v[158:161], v[58:61]
	v_mfma_f32_16x16x32_f16 v[54:57], v[170:173], v[136:139], v[54:57]
	v_mfma_f32_16x16x32_f16 v[50:53], v[170:173], v[158:161], v[50:53]
	v_mfma_f32_16x16x32_f16 v[46:49], v[178:181], v[136:139], v[46:49]
	v_mfma_f32_16x16x32_f16 v[42:45], v[178:181], v[158:161], v[42:45]
	v_mfma_f32_16x16x32_f16 v[38:41], v[186:189], v[136:139], v[38:41]
	v_mfma_f32_16x16x32_f16 v[34:37], v[186:189], v[158:161], v[34:37]
	v_mfma_f32_16x16x32_f16 v[62:65], v[166:169], v[140:143], v[62:65]
	v_mfma_f32_16x16x32_f16 v[58:61], v[166:169], v[162:165], v[58:61]
	v_mfma_f32_16x16x32_f16 v[54:57], v[174:177], v[140:143], v[54:57]
	v_mfma_f32_16x16x32_f16 v[50:53], v[174:177], v[162:165], v[50:53]
	v_mfma_f32_16x16x32_f16 v[46:49], v[182:185], v[140:143], v[46:49]
	v_mfma_f32_16x16x32_f16 v[42:45], v[182:185], v[162:165], v[42:45]
	v_mfma_f32_16x16x32_f16 v[38:41], v[190:193], v[140:143], v[38:41]
	v_mfma_f32_16x16x32_f16 v[34:37], v[190:193], v[162:165], v[34:37]
	s_setprio 1
	s_setprio 2
	v_mfma_f32_16x16x32_f16 v[30:33], v[130:133], v[196:199], v[30:33]
	v_mfma_f32_16x16x32_f16 v[26:29], v[130:133], v[204:207], v[26:29]
	v_mfma_f32_16x16x32_f16 v[22:25], v[170:173], v[196:199], v[22:25]
	v_mfma_f32_16x16x32_f16 v[18:21], v[170:173], v[204:207], v[18:21]
	v_mfma_f32_16x16x32_f16 v[14:17], v[178:181], v[196:199], v[14:17]
	v_mfma_f32_16x16x32_f16 v[10:13], v[178:181], v[204:207], v[10:13]
	v_mfma_f32_16x16x32_f16 v[6:9], v[186:189], v[196:199], v[6:9]
	v_mfma_f32_16x16x32_f16 v[2:5], v[186:189], v[204:207], v[2:5]
	v_mfma_f32_16x16x32_f16 v[30:33], v[166:169], v[200:203], v[30:33]
	v_mfma_f32_16x16x32_f16 v[26:29], v[166:169], v[208:211], v[26:29]
	v_mfma_f32_16x16x32_f16 v[22:25], v[174:177], v[200:203], v[22:25]
	v_mfma_f32_16x16x32_f16 v[18:21], v[174:177], v[208:211], v[18:21]
	v_mfma_f32_16x16x32_f16 v[14:17], v[182:185], v[200:203], v[14:17]
	v_mfma_f32_16x16x32_f16 v[10:13], v[182:185], v[208:211], v[10:13]
	v_mfma_f32_16x16x32_f16 v[6:9], v[190:193], v[200:203], v[6:9]
	v_mfma_f32_16x16x32_f16 v[2:5], v[190:193], v[208:211], v[2:5]
	s_setprio 1
	s_barrier
	ds_read_b128 v[130:133], v157
	ds_read_b128 v[134:137], v157 offset:1024
	ds_read_b128 v[138:141], v157 offset:2048
	ds_read_b128 v[156:159], v157 offset:3072
	ds_read_b128 v[160:163], v151 offset:32768
	ds_read_b128 v[164:167], v151 offset:33792
	ds_read_b128 v[168:171], v150 offset:32768
	ds_read_b128 v[172:175], v150 offset:33792
	ds_read_b128 v[176:179], v149 offset:32768
	ds_read_b128 v[180:183], v149 offset:33792
	ds_read_b128 v[184:187], v148 offset:32768
	ds_read_b128 v[188:191], v148 offset:33792
	s_waitcnt vmcnt(2)
	s_barrier
	s_waitcnt lgkmcnt(0)
	s_setprio 2
	s_waitcnt lgkmcnt(0)
	v_mfma_f32_16x16x32_f16 v[126:129], v[160:163], v[130:133], v[126:129]
	v_mfma_f32_16x16x32_f16 v[122:125], v[160:163], v[138:141], v[122:125]
	v_mfma_f32_16x16x32_f16 v[118:121], v[168:171], v[130:133], v[118:121]
	v_mfma_f32_16x16x32_f16 v[114:117], v[168:171], v[138:141], v[114:117]
	v_mfma_f32_16x16x32_f16 v[110:113], v[176:179], v[130:133], v[110:113]
	v_mfma_f32_16x16x32_f16 v[106:109], v[176:179], v[138:141], v[106:109]
	v_mfma_f32_16x16x32_f16 v[102:105], v[184:187], v[130:133], v[102:105]
	v_mfma_f32_16x16x32_f16 v[98:101], v[184:187], v[138:141], v[98:101]
	v_mfma_f32_16x16x32_f16 v[126:129], v[164:167], v[134:137], v[126:129]
	v_mfma_f32_16x16x32_f16 v[122:125], v[164:167], v[156:159], v[122:125]
	v_mfma_f32_16x16x32_f16 v[118:121], v[172:175], v[134:137], v[118:121]
	v_mfma_f32_16x16x32_f16 v[114:117], v[172:175], v[156:159], v[114:117]
	v_mfma_f32_16x16x32_f16 v[110:113], v[180:183], v[134:137], v[110:113]
	v_mfma_f32_16x16x32_f16 v[106:109], v[180:183], v[156:159], v[106:109]
	v_mfma_f32_16x16x32_f16 v[102:105], v[188:191], v[134:137], v[102:105]
	v_mfma_f32_16x16x32_f16 v[98:101], v[188:191], v[156:159], v[98:101]
	s_setprio 1
	s_barrier
	ds_read_b128 v[192:195], v154
	ds_read_b128 v[196:199], v154 offset:1024
	ds_read_b128 v[200:203], v154 offset:2048
	ds_read_b128 v[152:155], v154 offset:3072
	s_waitcnt vmcnt(0)
	s_barrier
	s_waitcnt lgkmcnt(0)
	s_setprio 2
	s_waitcnt lgkmcnt(0)
	v_mfma_f32_16x16x32_f16 v[94:97], v[160:163], v[192:195], v[94:97]
	v_mfma_f32_16x16x32_f16 v[90:93], v[160:163], v[200:203], v[90:93]
	v_mfma_f32_16x16x32_f16 v[86:89], v[168:171], v[192:195], v[86:89]
	v_mfma_f32_16x16x32_f16 v[82:85], v[168:171], v[200:203], v[82:85]
	v_mfma_f32_16x16x32_f16 v[78:81], v[176:179], v[192:195], v[78:81]
	v_mfma_f32_16x16x32_f16 v[74:77], v[176:179], v[200:203], v[74:77]
	v_mfma_f32_16x16x32_f16 v[70:73], v[184:187], v[192:195], v[70:73]
	v_mfma_f32_16x16x32_f16 v[66:69], v[184:187], v[200:203], v[66:69]
	v_mfma_f32_16x16x32_f16 v[94:97], v[164:167], v[196:199], v[94:97]
	v_mfma_f32_16x16x32_f16 v[90:93], v[164:167], v[152:155], v[90:93]
	v_mfma_f32_16x16x32_f16 v[86:89], v[172:175], v[196:199], v[86:89]
	v_mfma_f32_16x16x32_f16 v[82:85], v[172:175], v[152:155], v[82:85]
	v_mfma_f32_16x16x32_f16 v[78:81], v[180:183], v[196:199], v[78:81]
	v_mfma_f32_16x16x32_f16 v[74:77], v[180:183], v[152:155], v[74:77]
	v_mfma_f32_16x16x32_f16 v[70:73], v[188:191], v[196:199], v[70:73]
	v_mfma_f32_16x16x32_f16 v[66:69], v[188:191], v[152:155], v[66:69]
	s_setprio 1
	s_barrier
	ds_read_b128 v[160:163], v151 offset:49152
	ds_read_b128 v[164:167], v151 offset:50176
	ds_read_b128 v[168:171], v150 offset:49152
	ds_read_b128 v[172:175], v150 offset:50176
	ds_read_b128 v[176:179], v149 offset:49152
	ds_read_b128 v[180:183], v149 offset:50176
	ds_read_b128 v[184:187], v148 offset:49152
	ds_read_b128 v[148:151], v148 offset:50176
	s_barrier
	s_waitcnt lgkmcnt(0)
	s_setprio 2
	s_waitcnt lgkmcnt(0)
	v_mfma_f32_16x16x32_f16 v[62:65], v[160:163], v[130:133], v[62:65]
	v_mfma_f32_16x16x32_f16 v[58:61], v[160:163], v[138:141], v[58:61]
	v_mfma_f32_16x16x32_f16 v[54:57], v[168:171], v[130:133], v[54:57]
	v_mfma_f32_16x16x32_f16 v[50:53], v[168:171], v[138:141], v[50:53]
	v_mfma_f32_16x16x32_f16 v[46:49], v[176:179], v[130:133], v[46:49]
	v_mfma_f32_16x16x32_f16 v[42:45], v[176:179], v[138:141], v[42:45]
	v_mfma_f32_16x16x32_f16 v[38:41], v[184:187], v[130:133], v[38:41]
	v_mfma_f32_16x16x32_f16 v[34:37], v[184:187], v[138:141], v[34:37]
	v_mfma_f32_16x16x32_f16 v[62:65], v[164:167], v[134:137], v[62:65]
	v_mfma_f32_16x16x32_f16 v[58:61], v[164:167], v[156:159], v[58:61]
	v_mfma_f32_16x16x32_f16 v[54:57], v[172:175], v[134:137], v[54:57]
	v_mfma_f32_16x16x32_f16 v[50:53], v[172:175], v[156:159], v[50:53]
	v_mfma_f32_16x16x32_f16 v[46:49], v[180:183], v[134:137], v[46:49]
	v_mfma_f32_16x16x32_f16 v[42:45], v[180:183], v[156:159], v[42:45]
	v_mfma_f32_16x16x32_f16 v[38:41], v[148:151], v[134:137], v[38:41]
	v_mfma_f32_16x16x32_f16 v[34:37], v[148:151], v[156:159], v[34:37]
	s_setprio 1
	s_setprio 2
	v_mfma_f32_16x16x32_f16 v[30:33], v[160:163], v[192:195], v[30:33]
	v_mfma_f32_16x16x32_f16 v[26:29], v[160:163], v[200:203], v[26:29]
	v_mfma_f32_16x16x32_f16 v[22:25], v[168:171], v[192:195], v[22:25]
	v_mfma_f32_16x16x32_f16 v[18:21], v[168:171], v[200:203], v[18:21]
	v_mfma_f32_16x16x32_f16 v[14:17], v[176:179], v[192:195], v[14:17]
	v_mfma_f32_16x16x32_f16 v[10:13], v[176:179], v[200:203], v[10:13]
	v_mfma_f32_16x16x32_f16 v[6:9], v[184:187], v[192:195], v[6:9]
	v_mfma_f32_16x16x32_f16 v[2:5], v[184:187], v[200:203], v[2:5]
	v_mfma_f32_16x16x32_f16 v[30:33], v[164:167], v[196:199], v[30:33]
	v_mfma_f32_16x16x32_f16 v[26:29], v[164:167], v[152:155], v[26:29]
	v_mfma_f32_16x16x32_f16 v[22:25], v[172:175], v[196:199], v[22:25]
	v_mfma_f32_16x16x32_f16 v[18:21], v[172:175], v[152:155], v[18:21]
	v_mfma_f32_16x16x32_f16 v[14:17], v[180:183], v[196:199], v[14:17]
	v_mfma_f32_16x16x32_f16 v[10:13], v[180:183], v[152:155], v[10:13]
	v_mfma_f32_16x16x32_f16 v[6:9], v[148:151], v[196:199], v[6:9]
	v_mfma_f32_16x16x32_f16 v[2:5], v[148:151], v[152:155], v[2:5]
	s_setprio 1
	s_setprio 0
.Lg8_merge:
	s_movk_i32 s0, 0x100
	v_cmp_gt_u32_e32 vcc, s0, v0
	s_barrier
	s_and_saveexec_b64 s[0:1], vcc
	s_cbranch_execz .LBB15_10
	s_barrier

	.amdhsa_kernel _Z5gemm8ILi0EEvPKtS1_ii7EpiArgs
		.amdhsa_group_segment_fixed_size 0
		.amdhsa_private_segment_fixed_size 0
		.amdhsa_kernarg_size 80
		.amdhsa_user_sgpr_count 2
		.amdhsa_user_sgpr_dispatch_ptr 0
		.amdhsa_user_sgpr_queue_ptr 0
		.amdhsa_user_sgpr_kernarg_segment_ptr 1
		.amdhsa_user_sgpr_dispatch_id 0
		.amdhsa_user_sgpr_kernarg_preload_length 0
		.amdhsa_user_sgpr_kernarg_preload_offset 0
		.amdhsa_user_sgpr_private_segment_size 0
		.amdhsa_uses_dynamic_stack 0
		.amdhsa_enable_private_segment 0
		.amdhsa_system_sgpr_workgroup_id_x 1
		.amdhsa_system_sgpr_workgroup_id_y 0
		.amdhsa_system_sgpr_workgroup_id_z 0
		.amdhsa_system_sgpr_workgroup_info 0
		.amdhsa_system_vgpr_workitem_id 0
		.amdhsa_next_free_vgpr 250
		.amdhsa_next_free_sgpr 46
		.amdhsa_accum_offset 252
		.amdhsa_reserve_vcc 1
		.amdhsa_float_round_mode_32 0
		.amdhsa_float_round_mode_16_64 0
		.amdhsa_float_denorm_mode_32 3
		.amdhsa_float_denorm_mode_16_64 3
		.amdhsa_dx10_clamp 1
		.amdhsa_ieee_mode 1
		.amdhsa_fp16_overflow 0
		.amdhsa_tg_split 0
		.amdhsa_exception_fp_ieee_invalid_op 0
		.amdhsa_exception_fp_denorm_src 0
		.amdhsa_exception_fp_ieee_div_zero 0
		.amdhsa_exception_fp_ieee_overflow 0
		.amdhsa_exception_fp_ieee_underflow 0
		.amdhsa_exception_fp_ieee_inexact 0
		.amdhsa_exception_int_div_zero 0
	.end_amdhsa_kernel

.Lfunc_end15:
	.size	_Z5gemm8ILi0EEvPKtS1_ii7EpiArgs, .Lfunc_end15-_Z5gemm8ILi0EEvPKtS1_ii7EpiArgs
	.set _Z5gemm8ILi0EEvPKtS1_ii7EpiArgs.num_vgpr, 250
	.set _Z5gemm8ILi0EEvPKtS1_ii7EpiArgs.num_agpr, 0
	.set _Z5gemm8ILi0EEvPKtS1_ii7EpiArgs.numbered_sgpr, 46
	.set _Z5gemm8ILi0EEvPKtS1_ii7EpiArgs.num_named_barrier, 0
	.set _Z5gemm8ILi0EEvPKtS1_ii7EpiArgs.private_seg_size, 0
	.set _Z5gemm8ILi0EEvPKtS1_ii7EpiArgs.uses_vcc, 1
	.set _Z5gemm8ILi0EEvPKtS1_ii7EpiArgs.uses_flat_scratch, 0
	.set _Z5gemm8ILi0EEvPKtS1_ii7EpiArgs.has_dyn_sized_stack, 0
	.set _Z5gemm8ILi0EEvPKtS1_ii7EpiArgs.has_recursion, 0
	.set _Z5gemm8ILi0EEvPKtS1_ii7EpiArgs.has_indirect_call, 0

amdhsa.kernels:
  - .agpr_count:     0
    .args:
      - .actual_access:  read_only
        .address_space:  global
        .offset:         0
        .size:           8
        .value_kind:     global_buffer
      - .actual_access:  read_only
        .address_space:  global
        .offset:         8
        .size:           8
        .value_kind:     global_buffer
      - .actual_access:  write_only
        .address_space:  global
        .offset:         16
        .size:           8
        .value_kind:     global_buffer
      - .offset:         24
        .size:           4
        .value_kind:     by_value
      - .offset:         28
        .size:           4
        .value_kind:     by_value
      - .offset:         32
        .size:           4
        .value_kind:     by_value
      - .offset:         36
        .size:           4
        .value_kind:     by_value
    .group_segment_fixed_size: 8256
    .kernarg_segment_align: 8
    .kernarg_segment_size: 40
    .language:       OpenCL C
    .language_version:
      - 2
      - 0
    .max_flat_workgroup_size: 256
    .name:           _Z14gemm_f32_naivePKfS0_Pfiiii
    .private_segment_fixed_size: 0
    .sgpr_count:     24
    .sgpr_spill_count: 0
    .symbol:         _Z14gemm_f32_naivePKfS0_Pfiiii.kd
    .uniform_work_group_size: 1
    .uses_dynamic_stack: false
    .vgpr_count:     76
    .vgpr_spill_count: 0
    .wavefront_size: 64
  - .agpr_count:     0
    .args:
      - .actual_access:  read_only
        .address_space:  global
        .offset:         0
        .size:           8
        .value_kind:     global_buffer
      - .actual_access:  write_only
        .address_space:  global
        .offset:         8
        .size:           8
        .value_kind:     global_buffer
      - .actual_access:  write_only
        .address_space:  global
        .offset:         16
        .size:           8
        .value_kind:     global_buffer
      - .actual_access:  write_only
        .address_space:  global
        .offset:         24
        .size:           8
        .value_kind:     global_buffer
      - .actual_access:  write_only
        .address_space:  global
        .offset:         32
        .size:           8
        .value_kind:     global_buffer
      - .actual_access:  write_only
        .address_space:  global
        .offset:         40
        .size:           8
        .value_kind:     global_buffer
      - .actual_access:  write_only
        .address_space:  global
        .offset:         48
        .size:           8
        .value_kind:     global_buffer
    .group_segment_fixed_size: 0
    .kernarg_segment_align: 8
    .kernarg_segment_size: 56
    .language:       OpenCL C
    .language_version:
      - 2
      - 0
    .max_flat_workgroup_size: 256
    .name:           _Z10post_naivePKfPtS1_S1_S1_S1_S1_
    .private_segment_fixed_size: 0
    .sgpr_count:     28
    .sgpr_spill_count: 0
    .symbol:         _Z10post_naivePKfPtS1_S1_S1_S1_S1_.kd
    .uniform_work_group_size: 1
    .uses_dynamic_stack: false
    .vgpr_count:     38
    .vgpr_spill_count: 0
    .wavefront_size: 64
  - .agpr_count:     0
    .args:
      - .actual_access:  read_only
        .address_space:  global
        .offset:         0
        .size:           8
        .value_kind:     global_buffer
      - .actual_access:  read_only
        .address_space:  global
        .offset:         8
        .size:           8
        .value_kind:     global_buffer
      - .actual_access:  read_only
        .address_space:  global
        .offset:         16
        .size:           8
        .value_kind:     global_buffer
      - .actual_access:  read_only
        .address_space:  global
        .offset:         24
        .size:           8
        .value_kind:     global_buffer
      - .actual_access:  read_only
        .address_space:  global
        .offset:         32
        .size:           8
        .value_kind:     global_buffer
      - .actual_access:  read_only
        .address_space:  global
        .offset:         40
        .size:           8
        .value_kind:     global_buffer
      - .actual_access:  read_only
        .address_space:  global
        .offset:         48
        .size:           8
        .value_kind:     global_buffer
      - .actual_access:  write_only
        .address_space:  global
        .offset:         56
        .size:           8
        .value_kind:     global_buffer
      - .actual_access:  write_only
        .address_space:  global
        .offset:         64
        .size:           8
        .value_kind:     global_buffer
      - .actual_access:  write_only
        .address_space:  global
        .offset:         72
        .size:           8
        .value_kind:     global_buffer
      - .actual_access:  write_only
        .address_space:  global
        .offset:         80
        .size:           8
        .value_kind:     global_buffer
    .group_segment_fixed_size: 1152
    .kernarg_segment_align: 8
    .kernarg_segment_size: 88
    .language:       OpenCL C
    .language_version:
      - 2
      - 0
    .max_flat_workgroup_size: 256
    .name:           _Z11gates_naivePKfS0_S0_S0_S0_S0_S0_PtS1_S1_S1_
    .private_segment_fixed_size: 0
    .sgpr_count:     32
    .sgpr_spill_count: 0
    .symbol:         _Z11gates_naivePKfS0_S0_S0_S0_S0_S0_PtS1_S1_S1_.kd
    .uniform_work_group_size: 1
    .uses_dynamic_stack: false
    .vgpr_count:     66
    .vgpr_spill_count: 0
    .wavefront_size: 64
  - .agpr_count:     0
    .args:
      - .actual_access:  read_only
        .address_space:  global
        .offset:         0
        .size:           8
        .value_kind:     global_buffer
      - .actual_access:  read_only
        .address_space:  global
        .offset:         8
        .size:           8
        .value_kind:     global_buffer
      - .actual_access:  read_only
        .address_space:  global
        .offset:         16
        .size:           8
        .value_kind:     global_buffer
      - .actual_access:  read_only
        .address_space:  global
        .offset:         24
        .size:           8
        .value_kind:     global_buffer
      - .actual_access:  read_only
        .address_space:  global
        .offset:         32
        .size:           8
        .value_kind:     global_buffer
      - .actual_access:  read_only
        .address_space:  global
        .offset:         40
        .size:           8
        .value_kind:     global_buffer
      - .actual_access:  read_only
        .address_space:  global
        .offset:         48
        .size:           8
        .value_kind:     global_buffer
      - .actual_access:  write_only
        .address_space:  global
        .offset:         56
        .size:           8
        .value_kind:     global_buffer
    .group_segment_fixed_size: 12560
    .kernarg_segment_align: 8
    .kernarg_segment_size: 64
    .language:       OpenCL C
    .language_version:
      - 2
      - 0
    .max_flat_workgroup_size: 256
    .name:           _Z10attn_naivePKtS0_S0_S0_S0_S0_PKfPf
    .private_segment_fixed_size: 0
    .sgpr_count:     33
    .sgpr_spill_count: 0
    .symbol:         _Z10attn_naivePKtS0_S0_S0_S0_S0_PKfPf.kd
    .uniform_work_group_size: 1
    .uses_dynamic_stack: false
    .vgpr_count:     82
    .vgpr_spill_count: 0
    .wavefront_size: 64
  - .agpr_count:     0
    .args:
      - .address_space:  global
        .offset:         0
        .size:           8
        .value_kind:     global_buffer
      - .address_space:  global
        .offset:         8
        .size:           8
        .value_kind:     global_buffer
      - .actual_access:  write_only
        .address_space:  global
        .offset:         16
        .size:           8
        .value_kind:     global_buffer
    .group_segment_fixed_size: 0
    .kernarg_segment_align: 8
    .kernarg_segment_size: 24
    .language:       OpenCL C
    .language_version:
      - 2
      - 0
    .max_flat_workgroup_size: 512
    .name:           _Z8gemm_outPKtS0_Pf
    .private_segment_fixed_size: 0
    .sgpr_count:     26
    .sgpr_spill_count: 0
    .symbol:         _Z8gemm_outPKtS0_Pf.kd
    .uniform_work_group_size: 1
    .uses_dynamic_stack: false
    .vgpr_count:     158
    .vgpr_spill_count: 0
    .wavefront_size: 64
  - .agpr_count:     0
    .args:
      - .address_space:  global
        .offset:         0
        .size:           8
        .value_kind:     global_buffer
      - .address_space:  global
        .offset:         8
        .size:           8
        .value_kind:     global_buffer
      - .actual_access:  write_only
        .address_space:  global
        .offset:         16
        .size:           8
        .value_kind:     global_buffer
    .group_segment_fixed_size: 0
    .kernarg_segment_align: 8
    .kernarg_segment_size: 24
    .language:       OpenCL C
    .language_version:
      - 2
      - 0
    .max_flat_workgroup_size: 512
    .name:           _Z9gemm_out2PKtS0_Pf
    .private_segment_fixed_size: 0
    .sgpr_count:     27
    .sgpr_spill_count: 0
    .symbol:         _Z9gemm_out2PKtS0_Pf.kd
    .uniform_work_group_size: 1
    .uses_dynamic_stack: false
    .vgpr_count:     146
    .vgpr_spill_count: 0
    .wavefront_size: 64
  - .agpr_count:     0
    .args:
      - .actual_access:  read_only
        .address_space:  global
        .offset:         0
        .size:           8
        .value_kind:     global_buffer
      - .actual_access:  write_only
        .address_space:  global
        .offset:         8
        .size:           8
        .value_kind:     global_buffer
    .group_segment_fixed_size: 0
    .kernarg_segment_align: 8
    .kernarg_segment_size: 16
    .language:       OpenCL C
    .language_version:
      - 2
      - 0
    .max_flat_workgroup_size: 256
    .name:           _Z6conv_xPKfPt
    .private_segment_fixed_size: 0
    .sgpr_count:     14
    .sgpr_spill_count: 0
    .symbol:         _Z6conv_xPKfPt.kd
    .uniform_work_group_size: 1
    .uses_dynamic_stack: false
    .vgpr_count:     12
    .vgpr_spill_count: 0
    .wavefront_size: 64
  - .agpr_count:     0
    .args:
      - .actual_access:  read_only
        .address_space:  global
        .offset:         0
        .size:           8
        .value_kind:     global_buffer
      - .actual_access:  read_only
        .address_space:  global
        .offset:         8
        .size:           8
        .value_kind:     global_buffer
      - .actual_access:  read_only
        .address_space:  global
        .offset:         16
        .size:           8
        .value_kind:     global_buffer
      - .actual_access:  read_only
        .address_space:  global
        .offset:         24
        .size:           8
        .value_kind:     global_buffer
      - .actual_access:  read_only
        .address_space:  global
        .offset:         32
        .size:           8
        .value_kind:     global_buffer
      - .actual_access:  write_only
        .address_space:  global
        .offset:         40
        .size:           8
        .value_kind:     global_buffer
      - .actual_access:  write_only
        .address_space:  global
        .offset:         48
        .size:           8
        .value_kind:     global_buffer
    .group_segment_fixed_size: 16640
    .kernarg_segment_align: 8
    .kernarg_segment_size: 56
    .language:       OpenCL C
    .language_version:
      - 2
      - 0
    .max_flat_workgroup_size: 256
    .name:           _Z7conv_wTPKfS0_S0_S0_S0_PtS1_
    .private_segment_fixed_size: 0
    .sgpr_count:     26
    .sgpr_spill_count: 0
    .symbol:         _Z7conv_wTPKfS0_S0_S0_S0_PtS1_.kd
    .uniform_work_group_size: 1
    .uses_dynamic_stack: false
    .vgpr_count:     51
    .vgpr_spill_count: 0
    .wavefront_size: 64
  - .agpr_count:     0
    .args:
      - .actual_access:  read_only
        .address_space:  global
        .offset:         0
        .size:           8
        .value_kind:     global_buffer
      - .actual_access:  read_only
        .address_space:  global
        .offset:         8
        .size:           8
        .value_kind:     global_buffer
      - .actual_access:  write_only
        .address_space:  global
        .offset:         16
        .size:           8
        .value_kind:     global_buffer
    .group_segment_fixed_size: 0
    .kernarg_segment_align: 8
    .kernarg_segment_size: 24
    .language:       OpenCL C
    .language_version:
      - 2
      - 0
    .max_flat_workgroup_size: 256
    .name:           _Z7conv_w1PKfS0_Pt
    .private_segment_fixed_size: 0
    .sgpr_count:     16
    .sgpr_spill_count: 0
    .symbol:         _Z7conv_w1PKfS0_Pt.kd
    .uniform_work_group_size: 1
    .uses_dynamic_stack: false
    .vgpr_count:     6
    .vgpr_spill_count: 0
    .wavefront_size: 64
  - .agpr_count:     8
    .args:
      - .actual_access:  read_only
        .address_space:  global
        .offset:         0
        .size:           8
        .value_kind:     global_buffer
      - .actual_access:  read_only
        .address_space:  global
        .offset:         8
        .size:           8
        .value_kind:     global_buffer
      - .actual_access:  read_only
        .address_space:  global
        .offset:         16
        .size:           8
        .value_kind:     global_buffer
      - .actual_access:  read_only
        .address_space:  global
        .offset:         24
        .size:           8
        .value_kind:     global_buffer
      - .actual_access:  read_only
        .address_space:  global
        .offset:         32
        .size:           8
        .value_kind:     global_buffer
      - .actual_access:  read_only
        .address_space:  global
        .offset:         40
        .size:           8
        .value_kind:     global_buffer
      - .actual_access:  write_only
        .address_space:  global
        .offset:         48
        .size:           8
        .value_kind:     global_buffer
      - .actual_access:  write_only
        .address_space:  global
        .offset:         56
        .size:           8
        .value_kind:     global_buffer
      - .actual_access:  write_only
        .address_space:  global
        .offset:         64
        .size:           8
        .value_kind:     global_buffer
    .group_segment_fixed_size: 10240
    .kernarg_segment_align: 8
    .kernarg_segment_size: 72
    .language:       OpenCL C
    .language_version:
      - 2
      - 0
    .max_flat_workgroup_size: 256
    .name:           _Z10gates_fastPKtS0_PKfS2_S2_S2_PtS3_S3_
    .private_segment_fixed_size: 0
    .sgpr_count:     24
    .sgpr_spill_count: 0
    .symbol:         _Z10gates_fastPKtS0_PKfS2_S2_S2_PtS3_S3_.kd
    .uniform_work_group_size: 1
    .uses_dynamic_stack: false
    .vgpr_count:     96
    .vgpr_spill_count: 0
    .wavefront_size: 64
  - .agpr_count:     4
    .args:
      - .actual_access:  read_only
        .address_space:  global
        .offset:         0
        .size:           8
        .value_kind:     global_buffer
      - .actual_access:  read_only
        .address_space:  global
        .offset:         8
        .size:           8
        .value_kind:     global_buffer
      - .actual_access:  read_only
        .address_space:  global
        .offset:         16
        .size:           8
        .value_kind:     global_buffer
      - .actual_access:  read_only
        .address_space:  global
        .offset:         24
        .size:           8
        .value_kind:     global_buffer
      - .actual_access:  write_only
        .address_space:  global
        .offset:         32
        .size:           8
        .value_kind:     global_buffer
      - .actual_access:  write_only
        .address_space:  global
        .offset:         40
        .size:           8
        .value_kind:     global_buffer
      - .actual_access:  write_only
        .address_space:  global
        .offset:         48
        .size:           8
        .value_kind:     global_buffer
    .group_segment_fixed_size: 0
    .kernarg_segment_align: 8
    .kernarg_segment_size: 56
    .language:       OpenCL C
    .language_version:
      - 2
      - 0
    .max_flat_workgroup_size: 256
    .name:           _Z10state_fastPKtS0_S0_S0_PtS1_Pf
    .private_segment_fixed_size: 0
    .sgpr_count:     20
    .sgpr_spill_count: 0
    .symbol:         _Z10state_fastPKtS0_S0_S0_PtS1_Pf.kd
    .uniform_work_group_size: 1
    .uses_dynamic_stack: false
    .vgpr_count:     184
    .vgpr_spill_count: 0
    .wavefront_size: 64
  - .agpr_count:     0
    .args:
      - .actual_access:  read_only
        .address_space:  global
        .offset:         0
        .size:           8
        .value_kind:     global_buffer
      - .actual_access:  read_only
        .address_space:  global
        .offset:         8
        .size:           8
        .value_kind:     global_buffer
      - .actual_access:  read_only
        .address_space:  global
        .offset:         16
        .size:           8
        .value_kind:     global_buffer
      - .actual_access:  write_only
        .address_space:  global
        .offset:         24
        .size:           8
        .value_kind:     global_buffer
      - .actual_access:  write_only
        .address_space:  global
        .offset:         32
        .size:           8
        .value_kind:     global_buffer
      - .actual_access:  write_only
        .address_space:  global
        .offset:         40
        .size:           8
        .value_kind:     global_buffer
    .group_segment_fixed_size: 0
    .kernarg_segment_align: 8
    .kernarg_segment_size: 48
    .language:       OpenCL C
    .language_version:
      - 2
      - 0
    .max_flat_workgroup_size: 256
    .name:           _Z11prefix_fastPKtS0_PKfPtS3_Pf
    .private_segment_fixed_size: 0
    .sgpr_count:     106
    .sgpr_spill_count: 41
    .symbol:         _Z11prefix_fastPKtS0_PKfPtS3_Pf.kd
    .uniform_work_group_size: 1
    .uses_dynamic_stack: false
    .vgpr_count:     205
    .vgpr_spill_count: 0
    .wavefront_size: 64
  - .agpr_count:     0
    .args:
      - .address_space:  global
        .offset:         0
        .size:           8
        .value_kind:     global_buffer
      - .address_space:  global
        .offset:         8
        .size:           8
        .value_kind:     global_buffer
      - .address_space:  global
        .offset:         16
        .size:           8
        .value_kind:     global_buffer
      - .actual_access:  read_only
        .address_space:  global
        .offset:         24
        .size:           8
        .value_kind:     global_buffer
      - .address_space:  global
        .offset:         32
        .size:           8
        .value_kind:     global_buffer
      - .address_space:  global
        .offset:         40
        .size:           8
        .value_kind:     global_buffer
      - .address_space:  global
        .offset:         48
        .size:           8
        .value_kind:     global_buffer
      - .address_space:  global
        .offset:         56
        .size:           8
        .value_kind:     global_buffer
      - .address_space:  global
        .offset:         64
        .size:           8
        .value_kind:     global_buffer
      - .address_space:  global
        .offset:         72
        .size:           8
        .value_kind:     global_buffer
      - .address_space:  global
        .offset:         80
        .size:           8
        .value_kind:     global_buffer
      - .actual_access:  write_only
        .address_space:  global
        .offset:         88
        .size:           8
        .value_kind:     global_buffer
    .group_segment_fixed_size: 0
    .kernarg_segment_align: 8
    .kernarg_segment_size: 96
    .language:       OpenCL C
    .language_version:
      - 2
      - 0
    .max_flat_workgroup_size: 512
    .name:           _Z9attn_fastPKtS0_S0_S0_S0_S0_S0_S0_S0_PKfS2_Pt
    .private_segment_fixed_size: 0
    .sgpr_count:     52
    .sgpr_spill_count: 0
    .symbol:         _Z9attn_fastPKtS0_S0_S0_S0_S0_S0_S0_S0_PKfS2_Pt.kd
    .uniform_work_group_size: 1
    .uses_dynamic_stack: false
    .vgpr_count:     224
    .vgpr_spill_count: 0
    .wavefront_size: 64
  - .agpr_count:     12
    .args:
      - .actual_access:  read_only
        .address_space:  global
        .offset:         0
        .size:           8
        .value_kind:     global_buffer
      - .actual_access:  read_only
        .address_space:  global
        .offset:         8
        .size:           8
        .value_kind:     global_buffer
      - .actual_access:  read_only
        .address_space:  global
        .offset:         16
        .size:           8
        .value_kind:     global_buffer
      - .actual_access:  read_only
        .address_space:  global
        .offset:         24
        .size:           8
        .value_kind:     global_buffer
      - .actual_access:  read_only
        .address_space:  global
        .offset:         32
        .size:           8
        .value_kind:     global_buffer
      - .actual_access:  read_only
        .address_space:  global
        .offset:         40
        .size:           8
        .value_kind:     global_buffer
      - .actual_access:  read_only
        .address_space:  global
        .offset:         48
        .size:           8
        .value_kind:     global_buffer
      - .actual_access:  read_only
        .address_space:  global
        .offset:         56
        .size:           8
        .value_kind:     global_buffer
      - .actual_access:  read_only
        .address_space:  global
        .offset:         64
        .size:           8
        .value_kind:     global_buffer
      - .actual_access:  read_only
        .address_space:  global
        .offset:         72
        .size:           8
        .value_kind:     global_buffer
      - .actual_access:  read_only
        .address_space:  global
        .offset:         80
        .size:           8
        .value_kind:     global_buffer
      - .actual_access:  read_only
        .address_space:  global
        .offset:         88
        .size:           8
        .value_kind:     global_buffer
      - .actual_access:  write_only
        .address_space:  global
        .offset:         96
        .size:           8
        .value_kind:     global_buffer
      - .actual_access:  write_only
        .address_space:  global
        .offset:         104
        .size:           8
        .value_kind:     global_buffer
      - .actual_access:  write_only
        .address_space:  global
        .offset:         112
        .size:           8
        .value_kind:     global_buffer
      - .actual_access:  write_only
        .address_space:  global
        .offset:         120
        .size:           8
        .value_kind:     global_buffer
      - .actual_access:  write_only
        .address_space:  global
        .offset:         128
        .size:           8
        .value_kind:     global_buffer
      - .actual_access:  write_only
        .address_space:  global
        .offset:         136
        .size:           8
        .value_kind:     global_buffer
    .group_segment_fixed_size: 16640
    .kernarg_segment_align: 8
    .kernarg_segment_size: 144
    .language:       OpenCL C
    .language_version:
      - 2
      - 0
    .max_flat_workgroup_size: 256
    .name:           _Z11prep_kernelPKfS0_S0_S0_S0_S0_S0_S0_S0_S0_S0_S0_PtS1_S1_S1_S1_S1_
    .private_segment_fixed_size: 0
    .sgpr_count:     46
    .sgpr_spill_count: 0
    .symbol:         _Z11prep_kernelPKfS0_S0_S0_S0_S0_S0_S0_S0_S0_S0_S0_PtS1_S1_S1_S1_S1_.kd
    .uniform_work_group_size: 1
    .uses_dynamic_stack: false
    .vgpr_count:     168
    .vgpr_spill_count: 0
    .wavefront_size: 64
  - .agpr_count:     0
    .args:
      - .address_space:  global
        .offset:         0
        .size:           8
        .value_kind:     global_buffer
      - .address_space:  global
        .offset:         8
        .size:           8
        .value_kind:     global_buffer
      - .offset:         16
        .size:           4
        .value_kind:     by_value
      - .offset:         20
        .size:           4
        .value_kind:     by_value
      - .offset:         24
        .size:           4
        .value_kind:     by_value
      - .offset:         28
        .size:           4
        .value_kind:     by_value
      - .address_space:  global
        .offset:         32
        .size:           8
        .value_kind:     global_buffer
    .group_segment_fixed_size: 0
    .kernarg_segment_align: 8
    .kernarg_segment_size: 40
    .language:       OpenCL C
    .language_version:
      - 2
      - 0
    .max_flat_workgroup_size: 1024
    .name:           _Z9dbg_cmp16PKtS0_iiffPf
    .private_segment_fixed_size: 0
    .sgpr_count:     18
    .sgpr_spill_count: 0
    .symbol:         _Z9dbg_cmp16PKtS0_iiffPf.kd
    .uniform_work_group_size: 1
    .uses_dynamic_stack: false
    .vgpr_count:     5
    .vgpr_spill_count: 0
    .wavefront_size: 64
  - .agpr_count:     0
    .args:
      - .address_space:  global
        .offset:         0
        .size:           8
        .value_kind:     global_buffer
      - .address_space:  global
        .offset:         8
        .size:           8
        .value_kind:     global_buffer
      - .offset:         16
        .size:           4
        .value_kind:     by_value
      - .offset:         20
        .size:           4
        .value_kind:     by_value
      - .offset:         24
        .size:           56
        .value_kind:     by_value
    .group_segment_fixed_size: 0
    .kernarg_segment_align: 8
    .kernarg_segment_size: 80
    .language:       OpenCL C
    .language_version:
      - 2
      - 0
    .max_flat_workgroup_size: 512
    .name:           _Z5gemm8ILi0EEvPKtS1_ii7EpiArgs
    .private_segment_fixed_size: 0
    .sgpr_count:     52
    .sgpr_spill_count: 0
    .symbol:         _Z5gemm8ILi0EEvPKtS1_ii7EpiArgs.kd
    .uniform_work_group_size: 1
    .uses_dynamic_stack: false
    .vgpr_count:     250
    .vgpr_spill_count: 0
    .wavefront_size: 64
  - .agpr_count:     0
    .args:
      - .address_space:  global
        .offset:         0
        .size:           8
        .value_kind:     global_buffer
      - .address_space:  global
        .offset:         8
        .size:           8
        .value_kind:     global_buffer
      - .address_space:  global
        .offset:         16
        .size:           8
        .value_kind:     global_buffer
      - .address_space:  global
        .offset:         24
        .size:           8
        .value_kind:     global_buffer
      - .actual_access:  write_only
        .address_space:  global
        .offset:         32
        .size:           8
        .value_kind:     global_buffer
      - .actual_access:  write_only
        .address_space:  global
        .offset:         40
        .size:           8
        .value_kind:     global_buffer
      - .actual_access:  write_only
        .address_space:  global
        .offset:         48
        .size:           8
        .value_kind:     global_buffer
    .group_segment_fixed_size: 81920
    .kernarg_segment_align: 8
    .kernarg_segment_size: 56
    .language:       OpenCL C
    .language_version:
      - 2
      - 0
    .max_flat_workgroup_size: 256
    .name:           _Z9scan_fastILb1EEvPKtS1_S1_S1_PtS2_Pf
    .private_segment_fixed_size: 0
    .sgpr_count:     62
    .sgpr_spill_count: 0
    .symbol:         _Z9scan_fastILb1EEvPKtS1_S1_S1_PtS2_Pf.kd
    .uniform_work_group_size: 1
    .uses_dynamic_stack: false
    .vgpr_count:     160
    .vgpr_spill_count: 0
    .wavefront_size: 64
